# speedup vs baseline: 1.0153x; 1.0153x over previous
.LBB2_1:
	global_load_dwordx4 v[24:27], v[18:19], off offset:-8
	v_and_b32_e32 v23, 4, v22
	v_mad_u32_u24 v23, v23, s6, v17
	v_cmp_gt_u32_e32 vcc, 0x200, v0
	s_and_saveexec_b64 s[2:3], vcc
	v_lshl_add_u64 v[28:29], v[18:19], 0, s[4:5]
	v_add_u32_e32 v35, 0x800, v17
	global_load_dwordx4 v[30:33], v[28:29], off offset:-8
	v_and_b32_e32 v34, 4, v22
	v_mad_u32_u24 v34, v34, s6, v35
	s_mov_b64 exec, s[2:3]
	s_waitcnt vmcnt(0)
	ds_write_b32 v23, v24
	ds_write_b32 v23, v25 offset:3088
	ds_write_b32 v23, v26 offset:6176
	ds_write_b32 v23, v27 offset:9264
	s_and_saveexec_b64 s[2:3], vcc
	ds_write_b32 v34, v30
	ds_write_b32 v34, v31 offset:3088
	ds_write_b32 v34, v32 offset:6176
	ds_write_b32 v34, v33 offset:9264
	s_mov_b64 exec, s[2:3]
	s_or_b64 exec, exec, s[2:3]
	v_add_f32_e32 v17, v10, v11
	v_mov_b32_e32 v18, v6
	v_mov_b32_e32 v19, v2
	v_mov_b32_e32 v22, v7
	v_mov_b32_e32 v23, v3
	v_add_f32_e32 v17, v17, v12
	v_pk_add_f32 v[18:19], v[18:19], v[22:23]
	v_mov_b32_e32 v22, v8
	v_mov_b32_e32 v23, v4
	v_add_f32_e32 v17, v17, v13
	v_pk_add_f32 v[18:19], v[18:19], v[22:23]
	v_mov_b32_e32 v22, v9
	v_mov_b32_e32 v23, v5
	v_add_f32_e32 v17, 0, v17
	v_pk_add_f32 v[18:19], v[18:19], v[22:23]
	v_and_b32_e32 v22, 16, v0
	v_add_f32_e32 v17, v17, v18
	v_add_f32_e32 v17, v17, v19
	v_cmp_eq_u32_e64 s[4:5], 0, v22
	v_and_b32_e32 v22, 32, v0
	v_add_f32_dpp v17, v17, v17 quad_perm:[1,0,3,2] row_mask:0xf bank_mask:0xf bound_ctrl:1
	v_cmp_eq_u32_e64 s[2:3], 0, v22
	v_lshrrev_b32_e32 v1, 1, v0
	v_add_f32_dpp v17, v17, v17 quad_perm:[2,3,0,1] row_mask:0xf bank_mask:0xf bound_ctrl:1
	v_and_b32_e32 v1, 28, v1
	s_waitcnt lgkmcnt(0)
	v_add_f32_dpp v17, v17, v17 row_half_mirror row_mask:0xf bank_mask:0xf bound_ctrl:1
	s_barrier
	s_nop 0
	v_add_f32_dpp v17, v17, v17 row_mirror row_mask:0xf bank_mask:0xf bound_ctrl:1
	v_mov_b32_e32 v18, v17
	v_mov_b32_e32 v19, v17
	s_nop 1
	v_permlane16_swap_b32_e32 v18, v19
	v_cndmask_b32_e64 v18, v18, v19, s[4:5]
	v_add_f32_e32 v17, v17, v18
	v_mov_b32_e32 v18, v17
	v_mov_b32_e32 v19, v17
	s_nop 1
	v_permlane32_swap_b32_e32 v18, v19
	v_cndmask_b32_e64 v18, v18, v19, s[2:3]
	v_add_f32_e32 v17, v17, v18
	v_lshlrev_b32_e32 v18, 4, v16
	global_load_dword v1, v1, s[8:9]
	s_nop 0
	global_load_dwordx4 v[22:25], v18, s[18:19]
	global_load_dwordx4 v[26:29], v18, s[20:21]
	global_load_dwordx4 v[30:33], v18, s[18:19] offset:1024
	global_load_dwordx4 v[34:37], v18, s[20:21] offset:1024
	global_load_dwordx4 v[38:41], v18, s[18:19] offset:2048
	global_load_dwordx4 v[42:45], v18, s[20:21] offset:2048
	v_mul_f32_e32 v46, 0x3aaaaaab, v17
	v_pk_add_f32 v[10:11], v[10:11], v[46:47] op_sel_hi:[1,0] neg_lo:[0,1] neg_hi:[0,1]
	v_pk_add_f32 v[2:3], v[2:3], v[46:47] op_sel_hi:[1,0] neg_lo:[0,1] neg_hi:[0,1]
	v_pk_add_f32 v[6:7], v[6:7], v[46:47] op_sel_hi:[1,0] neg_lo:[0,1] neg_hi:[0,1]
	v_mov_b32_e32 v52, v3
	v_mov_b32_e32 v53, v11
	v_pk_add_f32 v[12:13], v[12:13], v[46:47] op_sel_hi:[1,0] neg_lo:[0,1] neg_hi:[0,1]
	v_pk_mul_f32 v[48:49], v[6:7], v[6:7]
	v_pk_add_f32 v[8:9], v[8:9], v[46:47] op_sel_hi:[1,0] neg_lo:[0,1] neg_hi:[0,1]
	v_pk_add_f32 v[4:5], v[4:5], v[46:47] op_sel_hi:[1,0] neg_lo:[0,1] neg_hi:[0,1]
	v_mov_b32_e32 v46, v2
	v_mov_b32_e32 v47, v10
	v_pk_mul_f32 v[52:53], v[52:53], v[52:53]
	v_pk_mul_f32 v[50:51], v[8:9], v[8:9]
	v_pk_fma_f32 v[46:47], v[46:47], v[46:47], v[52:53]
	v_mov_b32_e32 v52, v4
	v_mov_b32_e32 v53, v12
	v_add_f32_e32 v17, v48, v49
	v_mov_b32_e32 v54, v5
	v_mov_b32_e32 v55, v13
	v_pk_fma_f32 v[46:47], v[52:53], v[52:53], v[46:47]
	v_add_f32_e32 v17, v50, v17
	v_pk_fma_f32 v[46:47], v[54:55], v[54:55], v[46:47]
	v_add_f32_e32 v17, v51, v17
	v_add_f32_e32 v17, v47, v17
	v_add_f32_e32 v17, v46, v17
	s_mov_b32 s6, 0xf800000
	s_load_dword s0, s[0:1], 0x48
	v_add_f32_dpp v17, v17, v17 quad_perm:[1,0,3,2] row_mask:0xf bank_mask:0xf bound_ctrl:1
	s_waitcnt lgkmcnt(0)
	s_cmp_lg_u32 s0, 0
	v_add_f32_dpp v17, v17, v17 quad_perm:[2,3,0,1] row_mask:0xf bank_mask:0xf bound_ctrl:1
	s_nop 1
	v_add_f32_dpp v17, v17, v17 row_half_mirror row_mask:0xf bank_mask:0xf bound_ctrl:1
	s_nop 1
	v_add_f32_dpp v17, v17, v17 row_mirror row_mask:0xf bank_mask:0xf bound_ctrl:1
	v_mov_b32_e32 v19, v17
	v_mov_b32_e32 v46, v17
	s_nop 1
	v_permlane16_swap_b32_e32 v19, v46
	v_cndmask_b32_e64 v19, v19, v46, s[4:5]
	v_add_f32_e32 v17, v17, v19
	v_mov_b32_e32 v19, v17
	v_mov_b32_e32 v46, v17
	s_nop 1
	v_permlane32_swap_b32_e32 v19, v46
	v_cndmask_b32_e64 v19, v19, v46, s[2:3]
	v_add_f32_e32 v17, v17, v19
	v_mov_b32_e32 v19, 0x2b8cbccc
	v_fmac_f32_e32 v19, 0x3aaaaaab, v17
	v_mul_f32_e32 v17, 0x4f800000, v19
	v_cmp_gt_f32_e32 vcc, s6, v19
	s_nop 1
	v_cndmask_b32_e32 v17, v19, v17, vcc
	v_sqrt_f32_e32 v19, v17
	s_nop 0
	v_add_u32_e32 v46, -1, v19
	v_fma_f32 v47, -v46, v19, v17
	v_cmp_ge_f32_e64 s[6:7], 0, v47
	v_add_u32_e32 v47, 1, v19
	s_nop 0
	v_cndmask_b32_e64 v46, v19, v46, s[6:7]
	v_fma_f32 v19, -v47, v19, v17
	v_cmp_lt_f32_e64 s[6:7], 0, v19
	s_nop 1
	v_cndmask_b32_e64 v19, v46, v47, s[6:7]
	v_mul_f32_e32 v46, 0x37800000, v19
	v_cndmask_b32_e32 v19, v19, v46, vcc
	v_mov_b32_e32 v46, 0x260
	v_cmp_class_f32_e32 vcc, v17, v46
	s_nop 1
	v_cndmask_b32_e32 v17, v19, v17, vcc
	v_div_scale_f32 v19, s[6:7], v17, v17, 1.0
	v_rcp_f32_e32 v46, v19
	s_nop 0
	v_fma_f32 v47, -v19, v46, 1.0
	v_fmac_f32_e32 v46, v47, v46
	v_div_scale_f32 v47, vcc, 1.0, v17, 1.0
	v_mul_f32_e32 v48, v47, v46
	v_fma_f32 v49, -v19, v48, v47
	v_fmac_f32_e32 v48, v49, v46
	v_fma_f32 v19, -v19, v48, v47
	v_div_fmas_f32 v19, v19, v46, v48
	v_div_fixup_f32 v46, v19, v17, 1.0
	v_pk_mul_f32 v[10:11], v[10:11], v[46:47] op_sel_hi:[1,0]
	v_pk_mul_f32 v[12:13], v[12:13], v[46:47] op_sel_hi:[1,0]
	v_pk_mul_f32 v[6:7], v[6:7], v[46:47] op_sel_hi:[1,0]
	v_pk_mul_f32 v[8:9], v[8:9], v[46:47] op_sel_hi:[1,0]
	v_pk_mul_f32 v[2:3], v[2:3], v[46:47] op_sel_hi:[1,0]
	v_pk_mul_f32 v[4:5], v[4:5], v[46:47] op_sel_hi:[1,0]
	s_waitcnt vmcnt(4)
	v_pk_fma_f32 v[10:11], v[22:23], v[10:11], v[26:27]
	v_pk_fma_f32 v[12:13], v[24:25], v[12:13], v[28:29]
	s_waitcnt vmcnt(2)
	v_pk_fma_f32 v[6:7], v[6:7], v[30:31], v[34:35]
	v_pk_fma_f32 v[8:9], v[8:9], v[32:33], v[36:37]
	s_waitcnt vmcnt(0)
	v_pk_fma_f32 v[2:3], v[2:3], v[38:39], v[42:43]
	v_pk_fma_f32 v[4:5], v[4:5], v[40:41], v[44:45]
	s_cbranch_scc0 .LBB2_10
	v_and_b32_e32 v17, 0x1ff, v14
	v_cmp_eq_u32_e32 vcc, 0, v17
	s_and_saveexec_b64 s[0:1], vcc
	s_cbranch_execz .LBB2_5
	v_lshl_add_u64 v[22:23], s[10:11], 0, v[20:21]
	v_mov_b32_e32 v19, 0
	v_lshl_add_u64 v[22:23], v[22:23], 0, v[18:19]
	global_store_dwordx4 v[22:23], v[10:13], off
	global_store_dwordx4 v[22:23], v[6:9], off offset:1024
	global_store_dwordx4 v[22:23], v[2:5], off offset:2048

.LBB6_5:
	s_cmp_eq_u32 s3, 9
	s_mov_b64 s[10:11], -1
	s_cbranch_scc0 .LBB6_29
	s_branch .LBB6_4
	s_load_dword s21, s[0:1], 0x48
	s_lshl_b32 s20, s2, 8
	v_or_b32_e32 v2, s20, v0
	v_mov_b32_e32 v1, 0
	s_waitcnt lgkmcnt(0)
	v_cmp_gt_i32_e32 vcc, s21, v2
	s_and_saveexec_b64 s[10:11], vcc
	s_cbranch_execz .LBB6_16
	v_add_u32_e32 v1, 0x3000, v2
	v_max_i32_e32 v1, s21, v1
	v_sub_u32_e32 v1, v1, v0
	v_add_u32_e32 v1, 0xffffd000, v1
	v_cmp_ne_u32_e32 vcc, s20, v1
	s_mov_b32 s12, 0xaaaaaaab
	v_mov_b32_e32 v4, v2
	v_cndmask_b32_e64 v3, 0, 1, vcc
	v_or_b32_e32 v3, s20, v3
	v_sub_u32_e32 v1, v1, v3
	v_mul_hi_u32 v1, v1, s12
	v_lshrrev_b32_e32 v1, 13, v1
	v_addc_co_u32_e32 v5, vcc, 0, v1, vcc
	v_and_b32_e32 v1, 7, v5
	v_cmp_ne_u32_e32 vcc, 7, v1
	v_mov_b32_e32 v1, 0
	s_and_saveexec_b64 s[12:13], vcc
	s_cbranch_execz .LBB6_11
	v_add_u32_e32 v1, 1, v5
	v_ashrrev_i32_e32 v3, 31, v2
	v_and_b32_e32 v1, 7, v1
	v_lshl_add_u64 v[6:7], v[2:3], 4, s[14:15]
	v_lshl_add_u64 v[6:7], v[6:7], 0, 12
	v_sub_u32_e32 v3, 0, v1
	v_mov_b32_e32 v1, 0
	s_mov_b64 s[16:17], 0
	s_mov_b64 s[18:19], 0x30000
	v_mov_b32_e32 v4, v2

.LBB6_31:
	s_lshl_b32 s4, s3, 9
	s_ashr_i32 s5, s4, 31
	s_lshl_b64 s[0:1], s[4:5], 2
	s_waitcnt lgkmcnt(0)
	s_add_u32 s6, s46, s0
	s_addc_u32 s7, s47, s1
	s_load_dword s33, s[6:7], 0x0
	s_mul_hi_i32 s5, s4, 0xc00
	s_mulk_i32 s4, 0xc00
	s_add_u32 s4, s44, s4
	s_addc_u32 s5, s45, s5
	v_lshlrev_b32_e32 v6, 2, v0
	v_mov_b32_e32 v1, 0
	global_load_dword v2, v6, s[4:5]
	global_load_dword v3, v6, s[4:5] offset:1024
	global_load_dword v4, v6, s[4:5] offset:2048
	v_or_b32_e32 v5, 0x1000, v6
	s_mov_b64 s[0:1], exec
	s_waitcnt vmcnt(0)
	ds_write_b32 v5, v2
	ds_write_b32 v5, v3 offset:1024
	ds_write_b32 v5, v4 offset:2048

.LBB6_48:
	global_load_dword v64, v[6:7], off
	global_load_dword v65, v[8:9], off
	global_load_dword v66, v[4:5], off
	v_lshl_add_u64 v[4:5], v[4:5], 0, s[18:19]
	v_lshl_add_u64 v[6:7], v[6:7], 0, s[18:19]
	v_lshl_add_u64 v[8:9], v[8:9], 0, s[18:19]
	global_load_dword v67, v[6:7], off
	global_load_dword v68, v[8:9], off
	global_load_dword v69, v[4:5], off
	v_lshl_add_u64 v[4:5], v[4:5], 0, s[18:19]
	v_lshl_add_u64 v[6:7], v[6:7], 0, s[18:19]
	v_lshl_add_u64 v[8:9], v[8:9], 0, s[18:19]
	global_load_dword v70, v[6:7], off
	global_load_dword v71, v[8:9], off
	global_load_dword v72, v[4:5], off
	v_lshl_add_u64 v[4:5], v[4:5], 0, s[18:19]
	v_lshl_add_u64 v[6:7], v[6:7], 0, s[18:19]
	v_lshl_add_u64 v[8:9], v[8:9], 0, s[18:19]
	global_load_dword v73, v[6:7], off
	global_load_dword v74, v[8:9], off
	global_load_dword v75, v[4:5], off
	v_lshl_add_u64 v[4:5], v[4:5], 0, s[18:19]
	v_lshl_add_u64 v[6:7], v[6:7], 0, s[18:19]
	v_lshl_add_u64 v[8:9], v[8:9], 0, s[18:19]
	global_load_dword v76, v[6:7], off
	global_load_dword v77, v[8:9], off
	global_load_dword v78, v[4:5], off
	v_lshl_add_u64 v[4:5], v[4:5], 0, s[18:19]
	v_lshl_add_u64 v[6:7], v[6:7], 0, s[18:19]
	v_lshl_add_u64 v[8:9], v[8:9], 0, s[18:19]
	global_load_dword v79, v[6:7], off
	global_load_dword v80, v[8:9], off
	global_load_dword v81, v[4:5], off
	v_lshl_add_u64 v[4:5], v[4:5], 0, s[18:19]
	v_lshl_add_u64 v[6:7], v[6:7], 0, s[18:19]
	v_lshl_add_u64 v[8:9], v[8:9], 0, s[18:19]
	global_load_dword v82, v[6:7], off
	global_load_dword v83, v[8:9], off
	global_load_dword v84, v[4:5], off
	v_lshl_add_u64 v[4:5], v[4:5], 0, s[18:19]
	v_lshl_add_u64 v[6:7], v[6:7], 0, s[18:19]
	v_lshl_add_u64 v[8:9], v[8:9], 0, s[18:19]
	global_load_dword v85, v[6:7], off
	global_load_dword v86, v[8:9], off
	global_load_dword v87, v[4:5], off
	v_lshl_add_u64 v[4:5], v[4:5], 0, s[18:19]
	v_lshl_add_u64 v[6:7], v[6:7], 0, s[18:19]
	v_lshl_add_u64 v[8:9], v[8:9], 0, s[18:19]
	global_load_dword v88, v[6:7], off
	global_load_dword v89, v[8:9], off
	global_load_dword v90, v[4:5], off
	v_lshl_add_u64 v[4:5], v[4:5], 0, s[18:19]
	v_lshl_add_u64 v[6:7], v[6:7], 0, s[18:19]
	v_lshl_add_u64 v[8:9], v[8:9], 0, s[18:19]
	global_load_dword v91, v[6:7], off
	global_load_dword v92, v[8:9], off
	global_load_dword v93, v[4:5], off
	v_lshl_add_u64 v[4:5], v[4:5], 0, s[18:19]
	v_lshl_add_u64 v[6:7], v[6:7], 0, s[18:19]
	v_lshl_add_u64 v[8:9], v[8:9], 0, s[18:19]
	global_load_dword v94, v[6:7], off
	global_load_dword v95, v[8:9], off
	global_load_dword v96, v[4:5], off
	v_lshl_add_u64 v[4:5], v[4:5], 0, s[18:19]
	v_lshl_add_u64 v[6:7], v[6:7], 0, s[18:19]
	v_lshl_add_u64 v[8:9], v[8:9], 0, s[18:19]
	global_load_dword v97, v[6:7], off
	global_load_dword v98, v[8:9], off
	global_load_dword v99, v[4:5], off
	v_lshl_add_u64 v[4:5], v[4:5], 0, s[18:19]
	v_lshl_add_u64 v[6:7], v[6:7], 0, s[18:19]
	v_lshl_add_u64 v[8:9], v[8:9], 0, s[18:19]
	global_load_dword v100, v[6:7], off
	global_load_dword v101, v[8:9], off
	global_load_dword v102, v[4:5], off
	v_lshl_add_u64 v[4:5], v[4:5], 0, s[18:19]
	v_lshl_add_u64 v[6:7], v[6:7], 0, s[18:19]
	v_lshl_add_u64 v[8:9], v[8:9], 0, s[18:19]
	global_load_dword v103, v[6:7], off
	global_load_dword v104, v[8:9], off
	global_load_dword v105, v[4:5], off
	v_lshl_add_u64 v[4:5], v[4:5], 0, s[18:19]
	v_lshl_add_u64 v[6:7], v[6:7], 0, s[18:19]
	v_lshl_add_u64 v[8:9], v[8:9], 0, s[18:19]
	global_load_dword v106, v[6:7], off
	global_load_dword v107, v[8:9], off
	global_load_dword v108, v[4:5], off
	v_lshl_add_u64 v[4:5], v[4:5], 0, s[18:19]
	v_lshl_add_u64 v[6:7], v[6:7], 0, s[18:19]
	v_lshl_add_u64 v[8:9], v[8:9], 0, s[18:19]
	global_load_dword v109, v[6:7], off
	global_load_dword v110, v[8:9], off
	global_load_dword v111, v[4:5], off
	s_waitcnt vmcnt(45)
	v_cvt_f32_i32_e32 v64, v64
	v_cmp_eq_u32_e32 vcc, 1, v66
	v_cmp_eq_u32_e64 s[0:1], 2, v66
	v_fma_f32 v29, v65, v64, v25
	v_add_f32_e32 v30, v24, v64
	v_add_f32_e32 v31, v21, v64
	v_fma_f32 v32, v65, v64, v22
	v_add_f32_e32 v33, v19, v64
	v_fma_f32 v34, v65, v64, v20
	v_add_f32_e32 v35, v17, v64
	v_cmp_eq_u32_e64 s[4:5], 3, v66
	v_fma_f32 v36, v65, v64, v18
	v_add_f32_e32 v37, v15, v64
	v_cmp_eq_u32_e64 s[6:7], 4, v66
	v_fma_f32 v38, v65, v64, v16
	v_add_f32_e32 v39, v13, v64
	v_cmp_eq_u32_e64 s[8:9], 5, v66
	v_fma_f32 v40, v65, v64, v14
	v_add_f32_e32 v41, v11, v64
	v_cmp_eq_u32_e64 s[10:11], 6, v66
	v_fma_f32 v42, v65, v64, v12
	v_add_f32_e32 v43, v1, v64
	v_cmp_eq_u32_e64 s[12:13], 7, v66
	v_fma_f32 v65, v65, v64, v10
	v_cmp_eq_u32_e64 s[14:15], 0, v66
	v_add_f32_e32 v3, v3, v64
	v_cndmask_b32_e32 v21, v21, v31, vcc
	v_cndmask_b32_e64 v24, v24, v30, s[14:15]
	v_cndmask_b32_e64 v25, v25, v29, s[14:15]
	v_cndmask_b32_e32 v22, v22, v32, vcc
	v_cndmask_b32_e64 v19, v19, v33, s[0:1]
	v_cndmask_b32_e64 v20, v20, v34, s[0:1]
	v_cndmask_b32_e64 v17, v17, v35, s[4:5]
	v_cndmask_b32_e64 v18, v18, v36, s[4:5]
	v_cndmask_b32_e64 v15, v15, v37, s[6:7]
	v_cndmask_b32_e64 v16, v16, v38, s[6:7]
	v_cndmask_b32_e64 v13, v13, v39, s[8:9]
	v_cndmask_b32_e64 v14, v14, v40, s[8:9]
	v_cndmask_b32_e64 v11, v11, v41, s[10:11]
	v_cndmask_b32_e64 v12, v12, v42, s[10:11]
	v_cndmask_b32_e64 v1, v1, v43, s[12:13]
	v_cndmask_b32_e64 v10, v10, v65, s[12:13]
	s_waitcnt vmcnt(42)
	v_cvt_f32_i32_e32 v67, v67
	v_cmp_eq_u32_e32 vcc, 1, v69
	v_cmp_eq_u32_e64 s[0:1], 2, v69
	v_fma_f32 v29, v68, v67, v25
	v_add_f32_e32 v30, v24, v67
	v_add_f32_e32 v31, v21, v67
	v_fma_f32 v32, v68, v67, v22
	v_add_f32_e32 v33, v19, v67
	v_fma_f32 v34, v68, v67, v20
	v_add_f32_e32 v35, v17, v67
	v_cmp_eq_u32_e64 s[4:5], 3, v69
	v_fma_f32 v36, v68, v67, v18
	v_add_f32_e32 v37, v15, v67
	v_cmp_eq_u32_e64 s[6:7], 4, v69
	v_fma_f32 v38, v68, v67, v16
	v_add_f32_e32 v39, v13, v67
	v_cmp_eq_u32_e64 s[8:9], 5, v69
	v_fma_f32 v40, v68, v67, v14
	v_add_f32_e32 v41, v11, v67
	v_cmp_eq_u32_e64 s[10:11], 6, v69
	v_fma_f32 v42, v68, v67, v12
	v_add_f32_e32 v43, v1, v67
	v_cmp_eq_u32_e64 s[12:13], 7, v69
	v_fma_f32 v68, v68, v67, v10
	v_cmp_eq_u32_e64 s[14:15], 0, v69
	v_add_f32_e32 v3, v3, v67
	v_cndmask_b32_e32 v21, v21, v31, vcc
	v_cndmask_b32_e64 v24, v24, v30, s[14:15]
	v_cndmask_b32_e64 v25, v25, v29, s[14:15]
	v_cndmask_b32_e32 v22, v22, v32, vcc
	v_cndmask_b32_e64 v19, v19, v33, s[0:1]
	v_cndmask_b32_e64 v20, v20, v34, s[0:1]
	v_cndmask_b32_e64 v17, v17, v35, s[4:5]
	v_cndmask_b32_e64 v18, v18, v36, s[4:5]
	v_cndmask_b32_e64 v15, v15, v37, s[6:7]
	v_cndmask_b32_e64 v16, v16, v38, s[6:7]
	v_cndmask_b32_e64 v13, v13, v39, s[8:9]
	v_cndmask_b32_e64 v14, v14, v40, s[8:9]
	v_cndmask_b32_e64 v11, v11, v41, s[10:11]
	v_cndmask_b32_e64 v12, v12, v42, s[10:11]
	v_cndmask_b32_e64 v1, v1, v43, s[12:13]
	v_cndmask_b32_e64 v10, v10, v68, s[12:13]
	s_waitcnt vmcnt(39)
	v_cvt_f32_i32_e32 v70, v70
	v_cmp_eq_u32_e32 vcc, 1, v72
	v_cmp_eq_u32_e64 s[0:1], 2, v72
	v_fma_f32 v29, v71, v70, v25
	v_add_f32_e32 v30, v24, v70
	v_add_f32_e32 v31, v21, v70
	v_fma_f32 v32, v71, v70, v22
	v_add_f32_e32 v33, v19, v70
	v_fma_f32 v34, v71, v70, v20
	v_add_f32_e32 v35, v17, v70
	v_cmp_eq_u32_e64 s[4:5], 3, v72
	v_fma_f32 v36, v71, v70, v18
	v_add_f32_e32 v37, v15, v70
	v_cmp_eq_u32_e64 s[6:7], 4, v72
	v_fma_f32 v38, v71, v70, v16
	v_add_f32_e32 v39, v13, v70
	v_cmp_eq_u32_e64 s[8:9], 5, v72
	v_fma_f32 v40, v71, v70, v14
	v_add_f32_e32 v41, v11, v70
	v_cmp_eq_u32_e64 s[10:11], 6, v72
	v_fma_f32 v42, v71, v70, v12
	v_add_f32_e32 v43, v1, v70
	v_cmp_eq_u32_e64 s[12:13], 7, v72
	v_fma_f32 v71, v71, v70, v10
	v_cmp_eq_u32_e64 s[14:15], 0, v72
	v_add_f32_e32 v3, v3, v70
	v_cndmask_b32_e32 v21, v21, v31, vcc
	v_cndmask_b32_e64 v24, v24, v30, s[14:15]
	v_cndmask_b32_e64 v25, v25, v29, s[14:15]
	v_cndmask_b32_e32 v22, v22, v32, vcc
	v_cndmask_b32_e64 v19, v19, v33, s[0:1]
	v_cndmask_b32_e64 v20, v20, v34, s[0:1]
	v_cndmask_b32_e64 v17, v17, v35, s[4:5]
	v_cndmask_b32_e64 v18, v18, v36, s[4:5]
	v_cndmask_b32_e64 v15, v15, v37, s[6:7]
	v_cndmask_b32_e64 v16, v16, v38, s[6:7]
	v_cndmask_b32_e64 v13, v13, v39, s[8:9]
	v_cndmask_b32_e64 v14, v14, v40, s[8:9]
	v_cndmask_b32_e64 v11, v11, v41, s[10:11]
	v_cndmask_b32_e64 v12, v12, v42, s[10:11]
	v_cndmask_b32_e64 v1, v1, v43, s[12:13]
	v_cndmask_b32_e64 v10, v10, v71, s[12:13]
	s_waitcnt vmcnt(36)
	v_cvt_f32_i32_e32 v73, v73
	v_cmp_eq_u32_e32 vcc, 1, v75
	v_cmp_eq_u32_e64 s[0:1], 2, v75
	v_fma_f32 v29, v74, v73, v25
	v_add_f32_e32 v30, v24, v73
	v_add_f32_e32 v31, v21, v73
	v_fma_f32 v32, v74, v73, v22
	v_add_f32_e32 v33, v19, v73
	v_fma_f32 v34, v74, v73, v20
	v_add_f32_e32 v35, v17, v73
	v_cmp_eq_u32_e64 s[4:5], 3, v75
	v_fma_f32 v36, v74, v73, v18
	v_add_f32_e32 v37, v15, v73
	v_cmp_eq_u32_e64 s[6:7], 4, v75
	v_fma_f32 v38, v74, v73, v16
	v_add_f32_e32 v39, v13, v73
	v_cmp_eq_u32_e64 s[8:9], 5, v75
	v_fma_f32 v40, v74, v73, v14
	v_add_f32_e32 v41, v11, v73
	v_cmp_eq_u32_e64 s[10:11], 6, v75
	v_fma_f32 v42, v74, v73, v12
	v_add_f32_e32 v43, v1, v73
	v_cmp_eq_u32_e64 s[12:13], 7, v75
	v_fma_f32 v74, v74, v73, v10
	v_cmp_eq_u32_e64 s[14:15], 0, v75
	v_add_f32_e32 v3, v3, v73
	v_cndmask_b32_e32 v21, v21, v31, vcc
	v_cndmask_b32_e64 v24, v24, v30, s[14:15]
	v_cndmask_b32_e64 v25, v25, v29, s[14:15]
	v_cndmask_b32_e32 v22, v22, v32, vcc
	v_cndmask_b32_e64 v19, v19, v33, s[0:1]
	v_cndmask_b32_e64 v20, v20, v34, s[0:1]
	v_cndmask_b32_e64 v17, v17, v35, s[4:5]
	v_cndmask_b32_e64 v18, v18, v36, s[4:5]
	v_cndmask_b32_e64 v15, v15, v37, s[6:7]
	v_cndmask_b32_e64 v16, v16, v38, s[6:7]
	v_cndmask_b32_e64 v13, v13, v39, s[8:9]
	v_cndmask_b32_e64 v14, v14, v40, s[8:9]
	v_cndmask_b32_e64 v11, v11, v41, s[10:11]
	v_cndmask_b32_e64 v12, v12, v42, s[10:11]
	v_cndmask_b32_e64 v1, v1, v43, s[12:13]
	v_cndmask_b32_e64 v10, v10, v74, s[12:13]
	s_waitcnt vmcnt(33)
	v_cvt_f32_i32_e32 v76, v76
	v_cmp_eq_u32_e32 vcc, 1, v78
	v_cmp_eq_u32_e64 s[0:1], 2, v78
	v_fma_f32 v29, v77, v76, v25
	v_add_f32_e32 v30, v24, v76
	v_add_f32_e32 v31, v21, v76
	v_fma_f32 v32, v77, v76, v22
	v_add_f32_e32 v33, v19, v76
	v_fma_f32 v34, v77, v76, v20
	v_add_f32_e32 v35, v17, v76
	v_cmp_eq_u32_e64 s[4:5], 3, v78
	v_fma_f32 v36, v77, v76, v18
	v_add_f32_e32 v37, v15, v76
	v_cmp_eq_u32_e64 s[6:7], 4, v78
	v_fma_f32 v38, v77, v76, v16
	v_add_f32_e32 v39, v13, v76
	v_cmp_eq_u32_e64 s[8:9], 5, v78
	v_fma_f32 v40, v77, v76, v14
	v_add_f32_e32 v41, v11, v76
	v_cmp_eq_u32_e64 s[10:11], 6, v78
	v_fma_f32 v42, v77, v76, v12
	v_add_f32_e32 v43, v1, v76
	v_cmp_eq_u32_e64 s[12:13], 7, v78
	v_fma_f32 v77, v77, v76, v10
	v_cmp_eq_u32_e64 s[14:15], 0, v78
	v_add_f32_e32 v3, v3, v76
	v_cndmask_b32_e32 v21, v21, v31, vcc
	v_cndmask_b32_e64 v24, v24, v30, s[14:15]
	v_cndmask_b32_e64 v25, v25, v29, s[14:15]
	v_cndmask_b32_e32 v22, v22, v32, vcc
	v_cndmask_b32_e64 v19, v19, v33, s[0:1]
	v_cndmask_b32_e64 v20, v20, v34, s[0:1]
	v_cndmask_b32_e64 v17, v17, v35, s[4:5]
	v_cndmask_b32_e64 v18, v18, v36, s[4:5]
	v_cndmask_b32_e64 v15, v15, v37, s[6:7]
	v_cndmask_b32_e64 v16, v16, v38, s[6:7]
	v_cndmask_b32_e64 v13, v13, v39, s[8:9]
	v_cndmask_b32_e64 v14, v14, v40, s[8:9]
	v_cndmask_b32_e64 v11, v11, v41, s[10:11]
	v_cndmask_b32_e64 v12, v12, v42, s[10:11]
	v_cndmask_b32_e64 v1, v1, v43, s[12:13]
	v_cndmask_b32_e64 v10, v10, v77, s[12:13]
	s_waitcnt vmcnt(30)
	v_cvt_f32_i32_e32 v79, v79
	v_cmp_eq_u32_e32 vcc, 1, v81
	v_cmp_eq_u32_e64 s[0:1], 2, v81
	v_fma_f32 v29, v80, v79, v25
	v_add_f32_e32 v30, v24, v79
	v_add_f32_e32 v31, v21, v79
	v_fma_f32 v32, v80, v79, v22
	v_add_f32_e32 v33, v19, v79
	v_fma_f32 v34, v80, v79, v20
	v_add_f32_e32 v35, v17, v79
	v_cmp_eq_u32_e64 s[4:5], 3, v81
	v_fma_f32 v36, v80, v79, v18
	v_add_f32_e32 v37, v15, v79
	v_cmp_eq_u32_e64 s[6:7], 4, v81
	v_fma_f32 v38, v80, v79, v16
	v_add_f32_e32 v39, v13, v79
	v_cmp_eq_u32_e64 s[8:9], 5, v81
	v_fma_f32 v40, v80, v79, v14
	v_add_f32_e32 v41, v11, v79
	v_cmp_eq_u32_e64 s[10:11], 6, v81
	v_fma_f32 v42, v80, v79, v12
	v_add_f32_e32 v43, v1, v79
	v_cmp_eq_u32_e64 s[12:13], 7, v81
	v_fma_f32 v80, v80, v79, v10
	v_cmp_eq_u32_e64 s[14:15], 0, v81
	v_add_f32_e32 v3, v3, v79
	v_cndmask_b32_e32 v21, v21, v31, vcc
	v_cndmask_b32_e64 v24, v24, v30, s[14:15]
	v_cndmask_b32_e64 v25, v25, v29, s[14:15]
	v_cndmask_b32_e32 v22, v22, v32, vcc
	v_cndmask_b32_e64 v19, v19, v33, s[0:1]
	v_cndmask_b32_e64 v20, v20, v34, s[0:1]
	v_cndmask_b32_e64 v17, v17, v35, s[4:5]
	v_cndmask_b32_e64 v18, v18, v36, s[4:5]
	v_cndmask_b32_e64 v15, v15, v37, s[6:7]
	v_cndmask_b32_e64 v16, v16, v38, s[6:7]
	v_cndmask_b32_e64 v13, v13, v39, s[8:9]
	v_cndmask_b32_e64 v14, v14, v40, s[8:9]
	v_cndmask_b32_e64 v11, v11, v41, s[10:11]
	v_cndmask_b32_e64 v12, v12, v42, s[10:11]
	v_cndmask_b32_e64 v1, v1, v43, s[12:13]
	v_cndmask_b32_e64 v10, v10, v80, s[12:13]
	s_waitcnt vmcnt(27)
	v_cvt_f32_i32_e32 v82, v82
	v_cmp_eq_u32_e32 vcc, 1, v84
	v_cmp_eq_u32_e64 s[0:1], 2, v84
	v_fma_f32 v29, v83, v82, v25
	v_add_f32_e32 v30, v24, v82
	v_add_f32_e32 v31, v21, v82
	v_fma_f32 v32, v83, v82, v22
	v_add_f32_e32 v33, v19, v82
	v_fma_f32 v34, v83, v82, v20
	v_add_f32_e32 v35, v17, v82
	v_cmp_eq_u32_e64 s[4:5], 3, v84
	v_fma_f32 v36, v83, v82, v18
	v_add_f32_e32 v37, v15, v82
	v_cmp_eq_u32_e64 s[6:7], 4, v84
	v_fma_f32 v38, v83, v82, v16
	v_add_f32_e32 v39, v13, v82
	v_cmp_eq_u32_e64 s[8:9], 5, v84
	v_fma_f32 v40, v83, v82, v14
	v_add_f32_e32 v41, v11, v82
	v_cmp_eq_u32_e64 s[10:11], 6, v84
	v_fma_f32 v42, v83, v82, v12
	v_add_f32_e32 v43, v1, v82
	v_cmp_eq_u32_e64 s[12:13], 7, v84
	v_fma_f32 v83, v83, v82, v10
	v_cmp_eq_u32_e64 s[14:15], 0, v84
	v_add_f32_e32 v3, v3, v82
	v_cndmask_b32_e32 v21, v21, v31, vcc
	v_cndmask_b32_e64 v24, v24, v30, s[14:15]
	v_cndmask_b32_e64 v25, v25, v29, s[14:15]
	v_cndmask_b32_e32 v22, v22, v32, vcc
	v_cndmask_b32_e64 v19, v19, v33, s[0:1]
	v_cndmask_b32_e64 v20, v20, v34, s[0:1]
	v_cndmask_b32_e64 v17, v17, v35, s[4:5]
	v_cndmask_b32_e64 v18, v18, v36, s[4:5]
	v_cndmask_b32_e64 v15, v15, v37, s[6:7]
	v_cndmask_b32_e64 v16, v16, v38, s[6:7]
	v_cndmask_b32_e64 v13, v13, v39, s[8:9]
	v_cndmask_b32_e64 v14, v14, v40, s[8:9]
	v_cndmask_b32_e64 v11, v11, v41, s[10:11]
	v_cndmask_b32_e64 v12, v12, v42, s[10:11]
	v_cndmask_b32_e64 v1, v1, v43, s[12:13]
	v_cndmask_b32_e64 v10, v10, v83, s[12:13]
	s_waitcnt vmcnt(24)
	v_cvt_f32_i32_e32 v85, v85
	v_cmp_eq_u32_e32 vcc, 1, v87
	v_cmp_eq_u32_e64 s[0:1], 2, v87
	v_fma_f32 v29, v86, v85, v25
	v_add_f32_e32 v30, v24, v85
	v_add_f32_e32 v31, v21, v85
	v_fma_f32 v32, v86, v85, v22
	v_add_f32_e32 v33, v19, v85
	v_fma_f32 v34, v86, v85, v20
	v_add_f32_e32 v35, v17, v85
	v_cmp_eq_u32_e64 s[4:5], 3, v87
	v_fma_f32 v36, v86, v85, v18
	v_add_f32_e32 v37, v15, v85
	v_cmp_eq_u32_e64 s[6:7], 4, v87
	v_fma_f32 v38, v86, v85, v16
	v_add_f32_e32 v39, v13, v85
	v_cmp_eq_u32_e64 s[8:9], 5, v87
	v_fma_f32 v40, v86, v85, v14
	v_add_f32_e32 v41, v11, v85
	v_cmp_eq_u32_e64 s[10:11], 6, v87
	v_fma_f32 v42, v86, v85, v12
	v_add_f32_e32 v43, v1, v85
	v_cmp_eq_u32_e64 s[12:13], 7, v87
	v_fma_f32 v86, v86, v85, v10
	v_cmp_eq_u32_e64 s[14:15], 0, v87
	v_add_f32_e32 v3, v3, v85
	v_cndmask_b32_e32 v21, v21, v31, vcc
	v_cndmask_b32_e64 v24, v24, v30, s[14:15]
	v_cndmask_b32_e64 v25, v25, v29, s[14:15]
	v_cndmask_b32_e32 v22, v22, v32, vcc
	v_cndmask_b32_e64 v19, v19, v33, s[0:1]
	v_cndmask_b32_e64 v20, v20, v34, s[0:1]
	v_cndmask_b32_e64 v17, v17, v35, s[4:5]
	v_cndmask_b32_e64 v18, v18, v36, s[4:5]
	v_cndmask_b32_e64 v15, v15, v37, s[6:7]
	v_cndmask_b32_e64 v16, v16, v38, s[6:7]
	v_cndmask_b32_e64 v13, v13, v39, s[8:9]
	v_cndmask_b32_e64 v14, v14, v40, s[8:9]
	v_cndmask_b32_e64 v11, v11, v41, s[10:11]
	v_cndmask_b32_e64 v12, v12, v42, s[10:11]
	v_cndmask_b32_e64 v1, v1, v43, s[12:13]
	v_cndmask_b32_e64 v10, v10, v86, s[12:13]
	s_waitcnt vmcnt(21)
	v_cvt_f32_i32_e32 v88, v88
	v_cmp_eq_u32_e32 vcc, 1, v90
	v_cmp_eq_u32_e64 s[0:1], 2, v90
	v_fma_f32 v29, v89, v88, v25
	v_add_f32_e32 v30, v24, v88
	v_add_f32_e32 v31, v21, v88
	v_fma_f32 v32, v89, v88, v22
	v_add_f32_e32 v33, v19, v88
	v_fma_f32 v34, v89, v88, v20
	v_add_f32_e32 v35, v17, v88
	v_cmp_eq_u32_e64 s[4:5], 3, v90
	v_fma_f32 v36, v89, v88, v18
	v_add_f32_e32 v37, v15, v88
	v_cmp_eq_u32_e64 s[6:7], 4, v90
	v_fma_f32 v38, v89, v88, v16
	v_add_f32_e32 v39, v13, v88
	v_cmp_eq_u32_e64 s[8:9], 5, v90
	v_fma_f32 v40, v89, v88, v14
	v_add_f32_e32 v41, v11, v88
	v_cmp_eq_u32_e64 s[10:11], 6, v90
	v_fma_f32 v42, v89, v88, v12
	v_add_f32_e32 v43, v1, v88
	v_cmp_eq_u32_e64 s[12:13], 7, v90
	v_fma_f32 v89, v89, v88, v10
	v_cmp_eq_u32_e64 s[14:15], 0, v90
	v_add_f32_e32 v3, v3, v88
	v_cndmask_b32_e32 v21, v21, v31, vcc
	v_cndmask_b32_e64 v24, v24, v30, s[14:15]
	v_cndmask_b32_e64 v25, v25, v29, s[14:15]
	v_cndmask_b32_e32 v22, v22, v32, vcc
	v_cndmask_b32_e64 v19, v19, v33, s[0:1]
	v_cndmask_b32_e64 v20, v20, v34, s[0:1]
	v_cndmask_b32_e64 v17, v17, v35, s[4:5]
	v_cndmask_b32_e64 v18, v18, v36, s[4:5]
	v_cndmask_b32_e64 v15, v15, v37, s[6:7]
	v_cndmask_b32_e64 v16, v16, v38, s[6:7]
	v_cndmask_b32_e64 v13, v13, v39, s[8:9]
	v_cndmask_b32_e64 v14, v14, v40, s[8:9]
	v_cndmask_b32_e64 v11, v11, v41, s[10:11]
	v_cndmask_b32_e64 v12, v12, v42, s[10:11]
	v_cndmask_b32_e64 v1, v1, v43, s[12:13]
	v_cndmask_b32_e64 v10, v10, v89, s[12:13]
	s_waitcnt vmcnt(18)
	v_cvt_f32_i32_e32 v91, v91
	v_cmp_eq_u32_e32 vcc, 1, v93
	v_cmp_eq_u32_e64 s[0:1], 2, v93
	v_fma_f32 v29, v92, v91, v25
	v_add_f32_e32 v30, v24, v91
	v_add_f32_e32 v31, v21, v91
	v_fma_f32 v32, v92, v91, v22
	v_add_f32_e32 v33, v19, v91
	v_fma_f32 v34, v92, v91, v20
	v_add_f32_e32 v35, v17, v91
	v_cmp_eq_u32_e64 s[4:5], 3, v93
	v_fma_f32 v36, v92, v91, v18
	v_add_f32_e32 v37, v15, v91
	v_cmp_eq_u32_e64 s[6:7], 4, v93
	v_fma_f32 v38, v92, v91, v16
	v_add_f32_e32 v39, v13, v91
	v_cmp_eq_u32_e64 s[8:9], 5, v93
	v_fma_f32 v40, v92, v91, v14
	v_add_f32_e32 v41, v11, v91
	v_cmp_eq_u32_e64 s[10:11], 6, v93
	v_fma_f32 v42, v92, v91, v12
	v_add_f32_e32 v43, v1, v91
	v_cmp_eq_u32_e64 s[12:13], 7, v93
	v_fma_f32 v92, v92, v91, v10
	v_cmp_eq_u32_e64 s[14:15], 0, v93
	v_add_f32_e32 v3, v3, v91
	v_cndmask_b32_e32 v21, v21, v31, vcc
	v_cndmask_b32_e64 v24, v24, v30, s[14:15]
	v_cndmask_b32_e64 v25, v25, v29, s[14:15]
	v_cndmask_b32_e32 v22, v22, v32, vcc
	v_cndmask_b32_e64 v19, v19, v33, s[0:1]
	v_cndmask_b32_e64 v20, v20, v34, s[0:1]
	v_cndmask_b32_e64 v17, v17, v35, s[4:5]
	v_cndmask_b32_e64 v18, v18, v36, s[4:5]
	v_cndmask_b32_e64 v15, v15, v37, s[6:7]
	v_cndmask_b32_e64 v16, v16, v38, s[6:7]
	v_cndmask_b32_e64 v13, v13, v39, s[8:9]
	v_cndmask_b32_e64 v14, v14, v40, s[8:9]
	v_cndmask_b32_e64 v11, v11, v41, s[10:11]
	v_cndmask_b32_e64 v12, v12, v42, s[10:11]
	v_cndmask_b32_e64 v1, v1, v43, s[12:13]
	v_cndmask_b32_e64 v10, v10, v92, s[12:13]
	s_waitcnt vmcnt(15)
	v_cvt_f32_i32_e32 v94, v94
	v_cmp_eq_u32_e32 vcc, 1, v96
	v_cmp_eq_u32_e64 s[0:1], 2, v96
	v_fma_f32 v29, v95, v94, v25
	v_add_f32_e32 v30, v24, v94
	v_add_f32_e32 v31, v21, v94
	v_fma_f32 v32, v95, v94, v22
	v_add_f32_e32 v33, v19, v94
	v_fma_f32 v34, v95, v94, v20
	v_add_f32_e32 v35, v17, v94
	v_cmp_eq_u32_e64 s[4:5], 3, v96
	v_fma_f32 v36, v95, v94, v18
	v_add_f32_e32 v37, v15, v94
	v_cmp_eq_u32_e64 s[6:7], 4, v96
	v_fma_f32 v38, v95, v94, v16
	v_add_f32_e32 v39, v13, v94
	v_cmp_eq_u32_e64 s[8:9], 5, v96
	v_fma_f32 v40, v95, v94, v14
	v_add_f32_e32 v41, v11, v94
	v_cmp_eq_u32_e64 s[10:11], 6, v96
	v_fma_f32 v42, v95, v94, v12
	v_add_f32_e32 v43, v1, v94
	v_cmp_eq_u32_e64 s[12:13], 7, v96
	v_fma_f32 v95, v95, v94, v10
	v_cmp_eq_u32_e64 s[14:15], 0, v96
	v_add_f32_e32 v3, v3, v94
	v_cndmask_b32_e32 v21, v21, v31, vcc
	v_cndmask_b32_e64 v24, v24, v30, s[14:15]
	v_cndmask_b32_e64 v25, v25, v29, s[14:15]
	v_cndmask_b32_e32 v22, v22, v32, vcc
	v_cndmask_b32_e64 v19, v19, v33, s[0:1]
	v_cndmask_b32_e64 v20, v20, v34, s[0:1]
	v_cndmask_b32_e64 v17, v17, v35, s[4:5]
	v_cndmask_b32_e64 v18, v18, v36, s[4:5]
	v_cndmask_b32_e64 v15, v15, v37, s[6:7]
	v_cndmask_b32_e64 v16, v16, v38, s[6:7]
	v_cndmask_b32_e64 v13, v13, v39, s[8:9]
	v_cndmask_b32_e64 v14, v14, v40, s[8:9]
	v_cndmask_b32_e64 v11, v11, v41, s[10:11]
	v_cndmask_b32_e64 v12, v12, v42, s[10:11]
	v_cndmask_b32_e64 v1, v1, v43, s[12:13]
	v_cndmask_b32_e64 v10, v10, v95, s[12:13]
	s_waitcnt vmcnt(12)
	v_cvt_f32_i32_e32 v97, v97
	v_cmp_eq_u32_e32 vcc, 1, v99
	v_cmp_eq_u32_e64 s[0:1], 2, v99
	v_fma_f32 v29, v98, v97, v25
	v_add_f32_e32 v30, v24, v97
	v_add_f32_e32 v31, v21, v97
	v_fma_f32 v32, v98, v97, v22
	v_add_f32_e32 v33, v19, v97
	v_fma_f32 v34, v98, v97, v20
	v_add_f32_e32 v35, v17, v97
	v_cmp_eq_u32_e64 s[4:5], 3, v99
	v_fma_f32 v36, v98, v97, v18
	v_add_f32_e32 v37, v15, v97
	v_cmp_eq_u32_e64 s[6:7], 4, v99
	v_fma_f32 v38, v98, v97, v16
	v_add_f32_e32 v39, v13, v97
	v_cmp_eq_u32_e64 s[8:9], 5, v99
	v_fma_f32 v40, v98, v97, v14
	v_add_f32_e32 v41, v11, v97
	v_cmp_eq_u32_e64 s[10:11], 6, v99
	v_fma_f32 v42, v98, v97, v12
	v_add_f32_e32 v43, v1, v97
	v_cmp_eq_u32_e64 s[12:13], 7, v99
	v_fma_f32 v98, v98, v97, v10
	v_cmp_eq_u32_e64 s[14:15], 0, v99
	v_add_f32_e32 v3, v3, v97
	v_cndmask_b32_e32 v21, v21, v31, vcc
	v_cndmask_b32_e64 v24, v24, v30, s[14:15]
	v_cndmask_b32_e64 v25, v25, v29, s[14:15]
	v_cndmask_b32_e32 v22, v22, v32, vcc
	v_cndmask_b32_e64 v19, v19, v33, s[0:1]
	v_cndmask_b32_e64 v20, v20, v34, s[0:1]
	v_cndmask_b32_e64 v17, v17, v35, s[4:5]
	v_cndmask_b32_e64 v18, v18, v36, s[4:5]
	v_cndmask_b32_e64 v15, v15, v37, s[6:7]
	v_cndmask_b32_e64 v16, v16, v38, s[6:7]
	v_cndmask_b32_e64 v13, v13, v39, s[8:9]
	v_cndmask_b32_e64 v14, v14, v40, s[8:9]
	v_cndmask_b32_e64 v11, v11, v41, s[10:11]
	v_cndmask_b32_e64 v12, v12, v42, s[10:11]
	v_cndmask_b32_e64 v1, v1, v43, s[12:13]
	v_cndmask_b32_e64 v10, v10, v98, s[12:13]
	s_waitcnt vmcnt(9)
	v_cvt_f32_i32_e32 v100, v100
	v_cmp_eq_u32_e32 vcc, 1, v102
	v_cmp_eq_u32_e64 s[0:1], 2, v102
	v_fma_f32 v29, v101, v100, v25
	v_add_f32_e32 v30, v24, v100
	v_add_f32_e32 v31, v21, v100
	v_fma_f32 v32, v101, v100, v22
	v_add_f32_e32 v33, v19, v100
	v_fma_f32 v34, v101, v100, v20
	v_add_f32_e32 v35, v17, v100
	v_cmp_eq_u32_e64 s[4:5], 3, v102
	v_fma_f32 v36, v101, v100, v18
	v_add_f32_e32 v37, v15, v100
	v_cmp_eq_u32_e64 s[6:7], 4, v102
	v_fma_f32 v38, v101, v100, v16
	v_add_f32_e32 v39, v13, v100
	v_cmp_eq_u32_e64 s[8:9], 5, v102
	v_fma_f32 v40, v101, v100, v14
	v_add_f32_e32 v41, v11, v100
	v_cmp_eq_u32_e64 s[10:11], 6, v102
	v_fma_f32 v42, v101, v100, v12
	v_add_f32_e32 v43, v1, v100
	v_cmp_eq_u32_e64 s[12:13], 7, v102
	v_fma_f32 v101, v101, v100, v10
	v_cmp_eq_u32_e64 s[14:15], 0, v102
	v_add_f32_e32 v3, v3, v100
	v_cndmask_b32_e32 v21, v21, v31, vcc
	v_cndmask_b32_e64 v24, v24, v30, s[14:15]
	v_cndmask_b32_e64 v25, v25, v29, s[14:15]
	v_cndmask_b32_e32 v22, v22, v32, vcc
	v_cndmask_b32_e64 v19, v19, v33, s[0:1]
	v_cndmask_b32_e64 v20, v20, v34, s[0:1]
	v_cndmask_b32_e64 v17, v17, v35, s[4:5]
	v_cndmask_b32_e64 v18, v18, v36, s[4:5]
	v_cndmask_b32_e64 v15, v15, v37, s[6:7]
	v_cndmask_b32_e64 v16, v16, v38, s[6:7]
	v_cndmask_b32_e64 v13, v13, v39, s[8:9]
	v_cndmask_b32_e64 v14, v14, v40, s[8:9]
	v_cndmask_b32_e64 v11, v11, v41, s[10:11]
	v_cndmask_b32_e64 v12, v12, v42, s[10:11]
	v_cndmask_b32_e64 v1, v1, v43, s[12:13]
	v_cndmask_b32_e64 v10, v10, v101, s[12:13]
	s_waitcnt vmcnt(6)
	v_cvt_f32_i32_e32 v103, v103
	v_cmp_eq_u32_e32 vcc, 1, v105
	v_cmp_eq_u32_e64 s[0:1], 2, v105
	v_fma_f32 v29, v104, v103, v25
	v_add_f32_e32 v30, v24, v103
	v_add_f32_e32 v31, v21, v103
	v_fma_f32 v32, v104, v103, v22
	v_add_f32_e32 v33, v19, v103
	v_fma_f32 v34, v104, v103, v20
	v_add_f32_e32 v35, v17, v103
	v_cmp_eq_u32_e64 s[4:5], 3, v105
	v_fma_f32 v36, v104, v103, v18
	v_add_f32_e32 v37, v15, v103
	v_cmp_eq_u32_e64 s[6:7], 4, v105
	v_fma_f32 v38, v104, v103, v16
	v_add_f32_e32 v39, v13, v103
	v_cmp_eq_u32_e64 s[8:9], 5, v105
	v_fma_f32 v40, v104, v103, v14
	v_add_f32_e32 v41, v11, v103
	v_cmp_eq_u32_e64 s[10:11], 6, v105
	v_fma_f32 v42, v104, v103, v12
	v_add_f32_e32 v43, v1, v103
	v_cmp_eq_u32_e64 s[12:13], 7, v105
	v_fma_f32 v104, v104, v103, v10
	v_cmp_eq_u32_e64 s[14:15], 0, v105
	v_add_f32_e32 v3, v3, v103
	v_cndmask_b32_e32 v21, v21, v31, vcc
	v_cndmask_b32_e64 v24, v24, v30, s[14:15]
	v_cndmask_b32_e64 v25, v25, v29, s[14:15]
	v_cndmask_b32_e32 v22, v22, v32, vcc
	v_cndmask_b32_e64 v19, v19, v33, s[0:1]
	v_cndmask_b32_e64 v20, v20, v34, s[0:1]
	v_cndmask_b32_e64 v17, v17, v35, s[4:5]
	v_cndmask_b32_e64 v18, v18, v36, s[4:5]
	v_cndmask_b32_e64 v15, v15, v37, s[6:7]
	v_cndmask_b32_e64 v16, v16, v38, s[6:7]
	v_cndmask_b32_e64 v13, v13, v39, s[8:9]
	v_cndmask_b32_e64 v14, v14, v40, s[8:9]
	v_cndmask_b32_e64 v11, v11, v41, s[10:11]
	v_cndmask_b32_e64 v12, v12, v42, s[10:11]
	v_cndmask_b32_e64 v1, v1, v43, s[12:13]
	v_cndmask_b32_e64 v10, v10, v104, s[12:13]
	s_waitcnt vmcnt(3)
	v_cvt_f32_i32_e32 v106, v106
	v_cmp_eq_u32_e32 vcc, 1, v108
	v_cmp_eq_u32_e64 s[0:1], 2, v108
	v_fma_f32 v29, v107, v106, v25
	v_add_f32_e32 v30, v24, v106
	v_add_f32_e32 v31, v21, v106
	v_fma_f32 v32, v107, v106, v22
	v_add_f32_e32 v33, v19, v106
	v_fma_f32 v34, v107, v106, v20
	v_add_f32_e32 v35, v17, v106
	v_cmp_eq_u32_e64 s[4:5], 3, v108
	v_fma_f32 v36, v107, v106, v18
	v_add_f32_e32 v37, v15, v106
	v_cmp_eq_u32_e64 s[6:7], 4, v108
	v_fma_f32 v38, v107, v106, v16
	v_add_f32_e32 v39, v13, v106
	v_cmp_eq_u32_e64 s[8:9], 5, v108
	v_fma_f32 v40, v107, v106, v14
	v_add_f32_e32 v41, v11, v106
	v_cmp_eq_u32_e64 s[10:11], 6, v108
	v_fma_f32 v42, v107, v106, v12
	v_add_f32_e32 v43, v1, v106
	v_cmp_eq_u32_e64 s[12:13], 7, v108
	v_fma_f32 v107, v107, v106, v10
	v_cmp_eq_u32_e64 s[14:15], 0, v108
	v_add_f32_e32 v3, v3, v106
	v_cndmask_b32_e32 v21, v21, v31, vcc
	v_cndmask_b32_e64 v24, v24, v30, s[14:15]
	v_cndmask_b32_e64 v25, v25, v29, s[14:15]
	v_cndmask_b32_e32 v22, v22, v32, vcc
	v_cndmask_b32_e64 v19, v19, v33, s[0:1]
	v_cndmask_b32_e64 v20, v20, v34, s[0:1]
	v_cndmask_b32_e64 v17, v17, v35, s[4:5]
	v_cndmask_b32_e64 v18, v18, v36, s[4:5]
	v_cndmask_b32_e64 v15, v15, v37, s[6:7]
	v_cndmask_b32_e64 v16, v16, v38, s[6:7]
	v_cndmask_b32_e64 v13, v13, v39, s[8:9]
	v_cndmask_b32_e64 v14, v14, v40, s[8:9]
	v_cndmask_b32_e64 v11, v11, v41, s[10:11]
	v_cndmask_b32_e64 v12, v12, v42, s[10:11]
	v_cndmask_b32_e64 v1, v1, v43, s[12:13]
	v_cndmask_b32_e64 v10, v10, v107, s[12:13]
	s_waitcnt vmcnt(0)
	v_cvt_f32_i32_e32 v109, v109
	v_cmp_eq_u32_e32 vcc, 1, v111
	v_cmp_eq_u32_e64 s[0:1], 2, v111
	v_fma_f32 v29, v110, v109, v25
	v_add_f32_e32 v30, v24, v109
	v_add_f32_e32 v31, v21, v109
	v_fma_f32 v32, v110, v109, v22
	v_add_f32_e32 v33, v19, v109
	v_fma_f32 v34, v110, v109, v20
	v_add_f32_e32 v35, v17, v109
	v_cmp_eq_u32_e64 s[4:5], 3, v111
	v_fma_f32 v36, v110, v109, v18
	v_add_f32_e32 v37, v15, v109
	v_cmp_eq_u32_e64 s[6:7], 4, v111
	v_fma_f32 v38, v110, v109, v16
	v_add_f32_e32 v39, v13, v109
	v_cmp_eq_u32_e64 s[8:9], 5, v111
	v_fma_f32 v40, v110, v109, v14
	v_add_f32_e32 v41, v11, v109
	v_cmp_eq_u32_e64 s[10:11], 6, v111
	v_fma_f32 v42, v110, v109, v12
	v_add_f32_e32 v43, v1, v109
	v_cmp_eq_u32_e64 s[12:13], 7, v111
	v_fma_f32 v110, v110, v109, v10
	v_cmp_eq_u32_e64 s[14:15], 0, v111
	v_add_f32_e32 v3, v3, v109
	v_cndmask_b32_e32 v21, v21, v31, vcc
	v_cndmask_b32_e64 v24, v24, v30, s[14:15]
	v_cndmask_b32_e64 v25, v25, v29, s[14:15]
	v_cndmask_b32_e32 v22, v22, v32, vcc
	v_cndmask_b32_e64 v19, v19, v33, s[0:1]
	v_cndmask_b32_e64 v20, v20, v34, s[0:1]
	v_cndmask_b32_e64 v17, v17, v35, s[4:5]
	v_cndmask_b32_e64 v18, v18, v36, s[4:5]
	v_cndmask_b32_e64 v15, v15, v37, s[6:7]
	v_cndmask_b32_e64 v16, v16, v38, s[6:7]
	v_cndmask_b32_e64 v13, v13, v39, s[8:9]
	v_cndmask_b32_e64 v14, v14, v40, s[8:9]
	v_cndmask_b32_e64 v11, v11, v41, s[10:11]
	v_cndmask_b32_e64 v12, v12, v42, s[10:11]
	v_cndmask_b32_e64 v1, v1, v43, s[12:13]
	v_cndmask_b32_e64 v10, v10, v110, s[12:13]
	s_or_b64 exec, exec, s[16:17]
	v_and_b32_e32 v4, 63, v0
	v_cmp_eq_u32_e32 vcc, 0, v4
	v_and_b32_e32 v4, 32, v0
	v_cmp_eq_u32_e64 s[4:5], 0, v4
	v_and_b32_e32 v5, 16, v0
	v_add_f32_dpp v4, v25, v25 quad_perm:[1,0,3,2] row_mask:0xf bank_mask:0xf bound_ctrl:1
	v_cmp_eq_u32_e64 s[0:1], 0, v5
	v_and_b32_e32 v2, 0x300, v2
	v_add_f32_dpp v4, v4, v4 quad_perm:[2,3,0,1] row_mask:0xf bank_mask:0xf bound_ctrl:1
	s_nop 1
	v_add_f32_dpp v4, v4, v4 row_half_mirror row_mask:0xf bank_mask:0xf bound_ctrl:1
	s_nop 1
	v_add_f32_dpp v4, v4, v4 row_mirror row_mask:0xf bank_mask:0xf bound_ctrl:1
	v_mov_b32_e32 v6, v4
	v_mov_b32_e32 v7, v4
	s_nop 1
	v_permlane16_swap_b32_e32 v6, v7
	v_cndmask_b32_e64 v5, v6, v7, s[0:1]
	s_nop 0
	v_add_f32_dpp v7, v24, v24 quad_perm:[1,0,3,2] row_mask:0xf bank_mask:0xf bound_ctrl:1
	v_add_f32_e32 v4, v4, v5
	v_mov_b32_e32 v5, v4
	v_add_f32_dpp v7, v7, v7 quad_perm:[2,3,0,1] row_mask:0xf bank_mask:0xf bound_ctrl:1
	v_mov_b32_e32 v6, v4
	s_nop 1
	v_permlane32_swap_b32_e32 v5, v6
	v_add_f32_dpp v7, v7, v7 row_half_mirror row_mask:0xf bank_mask:0xf bound_ctrl:1
	s_nop 1
	v_add_f32_dpp v7, v7, v7 row_mirror row_mask:0xf bank_mask:0xf bound_ctrl:1
	v_mov_b32_e32 v8, v7
	v_mov_b32_e32 v9, v7
	s_nop 1
	v_permlane16_swap_b32_e32 v8, v9
	v_cndmask_b32_e64 v8, v8, v9, s[0:1]
	v_add_f32_e32 v7, v7, v8
	v_mov_b32_e32 v8, v7
	v_mov_b32_e32 v9, v7
	s_nop 1
	v_permlane32_swap_b32_e32 v8, v9
	s_and_saveexec_b64 s[6:7], vcc
	v_cndmask_b32_e64 v8, v8, v9, s[4:5]
	v_cndmask_b32_e64 v5, v5, v6, s[4:5]
	v_add_f32_e32 v7, v7, v8
	v_add_f32_e32 v4, v4, v5
	ds_write2_b32 v2, v4, v7 offset1:8
	s_or_b64 exec, exec, s[6:7]
	v_add_f32_dpp v4, v22, v22 quad_perm:[1,0,3,2] row_mask:0xf bank_mask:0xf bound_ctrl:1
	v_add_f32_dpp v7, v21, v21 quad_perm:[1,0,3,2] row_mask:0xf bank_mask:0xf bound_ctrl:1
	s_nop 0
	v_add_f32_dpp v4, v4, v4 quad_perm:[2,3,0,1] row_mask:0xf bank_mask:0xf bound_ctrl:1
	v_add_f32_dpp v7, v7, v7 quad_perm:[2,3,0,1] row_mask:0xf bank_mask:0xf bound_ctrl:1
	s_nop 0
	v_add_f32_dpp v4, v4, v4 row_half_mirror row_mask:0xf bank_mask:0xf bound_ctrl:1
	v_add_f32_dpp v7, v7, v7 row_half_mirror row_mask:0xf bank_mask:0xf bound_ctrl:1
	s_nop 0
	v_add_f32_dpp v4, v4, v4 row_mirror row_mask:0xf bank_mask:0xf bound_ctrl:1
	v_add_f32_dpp v7, v7, v7 row_mirror row_mask:0xf bank_mask:0xf bound_ctrl:1
	v_mov_b32_e32 v5, v4
	v_mov_b32_e32 v6, v4
	v_mov_b32_e32 v8, v7
	v_mov_b32_e32 v9, v7
	v_permlane16_swap_b32_e32 v5, v6
	s_nop 0
	v_permlane16_swap_b32_e32 v8, v9
	v_cndmask_b32_e64 v5, v5, v6, s[0:1]
	v_cndmask_b32_e64 v8, v8, v9, s[0:1]
	v_add_f32_e32 v4, v4, v5
	v_add_f32_e32 v7, v7, v8
	v_mov_b32_e32 v5, v4
	v_mov_b32_e32 v6, v4
	v_mov_b32_e32 v8, v7
	v_mov_b32_e32 v9, v7
	v_permlane32_swap_b32_e32 v5, v6
	s_nop 0
	v_permlane32_swap_b32_e32 v8, v9
	s_and_saveexec_b64 s[6:7], vcc
	v_cndmask_b32_e64 v8, v8, v9, s[4:5]
	v_cndmask_b32_e64 v5, v5, v6, s[4:5]
	v_add_f32_e32 v7, v7, v8
	v_add_f32_e32 v4, v4, v5
	ds_write2_b32 v2, v4, v7 offset0:1 offset1:9
	s_or_b64 exec, exec, s[6:7]
	v_add_f32_dpp v4, v20, v20 quad_perm:[1,0,3,2] row_mask:0xf bank_mask:0xf bound_ctrl:1
	v_add_f32_dpp v7, v19, v19 quad_perm:[1,0,3,2] row_mask:0xf bank_mask:0xf bound_ctrl:1
	s_nop 0
	v_add_f32_dpp v4, v4, v4 quad_perm:[2,3,0,1] row_mask:0xf bank_mask:0xf bound_ctrl:1
	v_add_f32_dpp v7, v7, v7 quad_perm:[2,3,0,1] row_mask:0xf bank_mask:0xf bound_ctrl:1
	s_nop 0
	v_add_f32_dpp v4, v4, v4 row_half_mirror row_mask:0xf bank_mask:0xf bound_ctrl:1
	v_add_f32_dpp v7, v7, v7 row_half_mirror row_mask:0xf bank_mask:0xf bound_ctrl:1
	s_nop 0
	v_add_f32_dpp v4, v4, v4 row_mirror row_mask:0xf bank_mask:0xf bound_ctrl:1
	v_add_f32_dpp v7, v7, v7 row_mirror row_mask:0xf bank_mask:0xf bound_ctrl:1
	v_mov_b32_e32 v5, v4
	v_mov_b32_e32 v6, v4
	v_mov_b32_e32 v8, v7
	v_mov_b32_e32 v9, v7
	v_permlane16_swap_b32_e32 v5, v6
	s_nop 0
	v_permlane16_swap_b32_e32 v8, v9
	v_cndmask_b32_e64 v5, v5, v6, s[0:1]
	v_cndmask_b32_e64 v8, v8, v9, s[0:1]
	v_add_f32_e32 v4, v4, v5
	v_add_f32_e32 v7, v7, v8
	v_mov_b32_e32 v5, v4
	v_mov_b32_e32 v6, v4
	v_mov_b32_e32 v8, v7
	v_mov_b32_e32 v9, v7
	v_permlane32_swap_b32_e32 v5, v6
	s_nop 0
	v_permlane32_swap_b32_e32 v8, v9
	s_and_saveexec_b64 s[6:7], vcc
	v_cndmask_b32_e64 v8, v8, v9, s[4:5]
	v_cndmask_b32_e64 v5, v5, v6, s[4:5]
	v_add_f32_e32 v7, v7, v8
	v_add_f32_e32 v4, v4, v5
	ds_write2_b32 v2, v4, v7 offset0:2 offset1:10
	s_or_b64 exec, exec, s[6:7]
	v_add_f32_dpp v4, v18, v18 quad_perm:[1,0,3,2] row_mask:0xf bank_mask:0xf bound_ctrl:1
	v_add_f32_dpp v7, v17, v17 quad_perm:[1,0,3,2] row_mask:0xf bank_mask:0xf bound_ctrl:1
	s_nop 0
	v_add_f32_dpp v4, v4, v4 quad_perm:[2,3,0,1] row_mask:0xf bank_mask:0xf bound_ctrl:1
	v_add_f32_dpp v7, v7, v7 quad_perm:[2,3,0,1] row_mask:0xf bank_mask:0xf bound_ctrl:1
	s_nop 0
	v_add_f32_dpp v4, v4, v4 row_half_mirror row_mask:0xf bank_mask:0xf bound_ctrl:1
	v_add_f32_dpp v7, v7, v7 row_half_mirror row_mask:0xf bank_mask:0xf bound_ctrl:1
	s_nop 0
	v_add_f32_dpp v4, v4, v4 row_mirror row_mask:0xf bank_mask:0xf bound_ctrl:1
	v_add_f32_dpp v7, v7, v7 row_mirror row_mask:0xf bank_mask:0xf bound_ctrl:1
	v_mov_b32_e32 v5, v4
	v_mov_b32_e32 v6, v4
	v_mov_b32_e32 v8, v7
	v_mov_b32_e32 v9, v7
	v_permlane16_swap_b32_e32 v5, v6
	s_nop 0
	v_permlane16_swap_b32_e32 v8, v9
	v_cndmask_b32_e64 v5, v5, v6, s[0:1]
	v_cndmask_b32_e64 v8, v8, v9, s[0:1]
	v_add_f32_e32 v4, v4, v5
	v_add_f32_e32 v7, v7, v8
	v_mov_b32_e32 v5, v4
	v_mov_b32_e32 v6, v4
	v_mov_b32_e32 v8, v7
	v_mov_b32_e32 v9, v7
	v_permlane32_swap_b32_e32 v5, v6
	s_nop 0
	v_permlane32_swap_b32_e32 v8, v9
	s_and_saveexec_b64 s[6:7], vcc
	v_cndmask_b32_e64 v8, v8, v9, s[4:5]
	v_cndmask_b32_e64 v5, v5, v6, s[4:5]
	v_add_f32_e32 v7, v7, v8
	v_add_f32_e32 v4, v4, v5
	ds_write2_b32 v2, v4, v7 offset0:3 offset1:11
	s_or_b64 exec, exec, s[6:7]
	v_add_f32_dpp v4, v16, v16 quad_perm:[1,0,3,2] row_mask:0xf bank_mask:0xf bound_ctrl:1
	v_add_f32_dpp v7, v15, v15 quad_perm:[1,0,3,2] row_mask:0xf bank_mask:0xf bound_ctrl:1
	s_nop 0
	v_add_f32_dpp v4, v4, v4 quad_perm:[2,3,0,1] row_mask:0xf bank_mask:0xf bound_ctrl:1
	v_add_f32_dpp v7, v7, v7 quad_perm:[2,3,0,1] row_mask:0xf bank_mask:0xf bound_ctrl:1
	s_nop 0
	v_add_f32_dpp v4, v4, v4 row_half_mirror row_mask:0xf bank_mask:0xf bound_ctrl:1
	v_add_f32_dpp v7, v7, v7 row_half_mirror row_mask:0xf bank_mask:0xf bound_ctrl:1
	s_nop 0
	v_add_f32_dpp v4, v4, v4 row_mirror row_mask:0xf bank_mask:0xf bound_ctrl:1
	v_add_f32_dpp v7, v7, v7 row_mirror row_mask:0xf bank_mask:0xf bound_ctrl:1
	v_mov_b32_e32 v5, v4
	v_mov_b32_e32 v6, v4
	v_mov_b32_e32 v8, v7
	v_mov_b32_e32 v9, v7
	v_permlane16_swap_b32_e32 v5, v6
	s_nop 0
	v_permlane16_swap_b32_e32 v8, v9
	v_cndmask_b32_e64 v5, v5, v6, s[0:1]
	v_cndmask_b32_e64 v8, v8, v9, s[0:1]
	v_add_f32_e32 v4, v4, v5
	v_add_f32_e32 v7, v7, v8
	v_mov_b32_e32 v5, v4
	v_mov_b32_e32 v6, v4
	v_mov_b32_e32 v8, v7
	v_mov_b32_e32 v9, v7
	v_permlane32_swap_b32_e32 v5, v6
	s_nop 0
	v_permlane32_swap_b32_e32 v8, v9
	s_and_saveexec_b64 s[6:7], vcc
	v_cndmask_b32_e64 v8, v8, v9, s[4:5]
	v_cndmask_b32_e64 v5, v5, v6, s[4:5]
	v_add_f32_e32 v7, v7, v8
	v_add_f32_e32 v4, v4, v5
	ds_write2_b32 v2, v4, v7 offset0:4 offset1:12
	s_or_b64 exec, exec, s[6:7]
	v_add_f32_dpp v4, v14, v14 quad_perm:[1,0,3,2] row_mask:0xf bank_mask:0xf bound_ctrl:1
	v_add_f32_dpp v7, v13, v13 quad_perm:[1,0,3,2] row_mask:0xf bank_mask:0xf bound_ctrl:1
	s_nop 0
	v_add_f32_dpp v4, v4, v4 quad_perm:[2,3,0,1] row_mask:0xf bank_mask:0xf bound_ctrl:1
	v_add_f32_dpp v7, v7, v7 quad_perm:[2,3,0,1] row_mask:0xf bank_mask:0xf bound_ctrl:1
	s_nop 0
	v_add_f32_dpp v4, v4, v4 row_half_mirror row_mask:0xf bank_mask:0xf bound_ctrl:1
	v_add_f32_dpp v7, v7, v7 row_half_mirror row_mask:0xf bank_mask:0xf bound_ctrl:1
	s_nop 0
	v_add_f32_dpp v4, v4, v4 row_mirror row_mask:0xf bank_mask:0xf bound_ctrl:1
	v_add_f32_dpp v7, v7, v7 row_mirror row_mask:0xf bank_mask:0xf bound_ctrl:1
	v_mov_b32_e32 v5, v4
	v_mov_b32_e32 v6, v4
	v_mov_b32_e32 v8, v7
	v_mov_b32_e32 v9, v7
	v_permlane16_swap_b32_e32 v5, v6
	s_nop 0
	v_permlane16_swap_b32_e32 v8, v9
	v_cndmask_b32_e64 v5, v5, v6, s[0:1]
	v_cndmask_b32_e64 v8, v8, v9, s[0:1]
	v_add_f32_e32 v4, v4, v5
	v_add_f32_e32 v7, v7, v8
	v_mov_b32_e32 v5, v4
	v_mov_b32_e32 v6, v4
	v_mov_b32_e32 v8, v7
	v_mov_b32_e32 v9, v7
	v_permlane32_swap_b32_e32 v5, v6
	s_nop 0
	v_permlane32_swap_b32_e32 v8, v9
	s_and_saveexec_b64 s[6:7], vcc
	v_cndmask_b32_e64 v8, v8, v9, s[4:5]
	v_cndmask_b32_e64 v5, v5, v6, s[4:5]
	v_add_f32_e32 v7, v7, v8
	v_add_f32_e32 v4, v4, v5
	ds_write2_b32 v2, v4, v7 offset0:5 offset1:13
	s_or_b64 exec, exec, s[6:7]
	v_add_f32_dpp v4, v12, v12 quad_perm:[1,0,3,2] row_mask:0xf bank_mask:0xf bound_ctrl:1
	v_add_f32_dpp v7, v11, v11 quad_perm:[1,0,3,2] row_mask:0xf bank_mask:0xf bound_ctrl:1
	s_nop 0
	v_add_f32_dpp v4, v4, v4 quad_perm:[2,3,0,1] row_mask:0xf bank_mask:0xf bound_ctrl:1
	v_add_f32_dpp v7, v7, v7 quad_perm:[2,3,0,1] row_mask:0xf bank_mask:0xf bound_ctrl:1
	s_nop 0
	v_add_f32_dpp v4, v4, v4 row_half_mirror row_mask:0xf bank_mask:0xf bound_ctrl:1
	v_add_f32_dpp v7, v7, v7 row_half_mirror row_mask:0xf bank_mask:0xf bound_ctrl:1
	s_nop 0
	v_add_f32_dpp v4, v4, v4 row_mirror row_mask:0xf bank_mask:0xf bound_ctrl:1
	v_add_f32_dpp v7, v7, v7 row_mirror row_mask:0xf bank_mask:0xf bound_ctrl:1
	v_mov_b32_e32 v5, v4
	v_mov_b32_e32 v6, v4
	v_mov_b32_e32 v8, v7
	v_mov_b32_e32 v9, v7
	v_permlane16_swap_b32_e32 v5, v6
	s_nop 0
	v_permlane16_swap_b32_e32 v8, v9
	v_cndmask_b32_e64 v5, v5, v6, s[0:1]
	v_cndmask_b32_e64 v8, v8, v9, s[0:1]
	v_add_f32_e32 v4, v4, v5
	v_add_f32_e32 v7, v7, v8
	v_mov_b32_e32 v5, v4
	v_mov_b32_e32 v6, v4
	v_mov_b32_e32 v8, v7
	v_mov_b32_e32 v9, v7
	v_permlane32_swap_b32_e32 v5, v6
	s_nop 0
	v_permlane32_swap_b32_e32 v8, v9
	s_and_saveexec_b64 s[6:7], vcc
	v_cndmask_b32_e64 v8, v8, v9, s[4:5]
	v_cndmask_b32_e64 v5, v5, v6, s[4:5]
	v_add_f32_e32 v7, v7, v8
	v_add_f32_e32 v4, v4, v5
	ds_write2_b32 v2, v4, v7 offset0:6 offset1:14
	s_or_b64 exec, exec, s[6:7]
	v_add_f32_dpp v4, v10, v10 quad_perm:[1,0,3,2] row_mask:0xf bank_mask:0xf bound_ctrl:1
	v_add_f32_dpp v1, v1, v1 quad_perm:[1,0,3,2] row_mask:0xf bank_mask:0xf bound_ctrl:1
	s_nop 0
	v_add_f32_dpp v4, v4, v4 quad_perm:[2,3,0,1] row_mask:0xf bank_mask:0xf bound_ctrl:1
	v_add_f32_dpp v1, v1, v1 quad_perm:[2,3,0,1] row_mask:0xf bank_mask:0xf bound_ctrl:1
	s_nop 0
	v_add_f32_dpp v4, v4, v4 row_half_mirror row_mask:0xf bank_mask:0xf bound_ctrl:1
	v_add_f32_dpp v1, v1, v1 row_half_mirror row_mask:0xf bank_mask:0xf bound_ctrl:1
	s_nop 0
	v_add_f32_dpp v4, v4, v4 row_mirror row_mask:0xf bank_mask:0xf bound_ctrl:1
	v_add_f32_dpp v1, v1, v1 row_mirror row_mask:0xf bank_mask:0xf bound_ctrl:1
	v_mov_b32_e32 v5, v4
	v_mov_b32_e32 v6, v4
	v_mov_b32_e32 v7, v1
	v_mov_b32_e32 v8, v1
	v_permlane16_swap_b32_e32 v5, v6
	s_nop 0
	v_permlane16_swap_b32_e32 v7, v8
	v_cndmask_b32_e64 v5, v5, v6, s[0:1]
	v_cndmask_b32_e64 v7, v7, v8, s[0:1]
	v_add_f32_e32 v4, v4, v5
	v_add_f32_e32 v1, v1, v7
	v_mov_b32_e32 v5, v4
	v_mov_b32_e32 v6, v4
	v_mov_b32_e32 v7, v1
	v_mov_b32_e32 v8, v1
	v_permlane32_swap_b32_e32 v5, v6
	s_nop 0
	v_permlane32_swap_b32_e32 v7, v8
	s_and_saveexec_b64 s[6:7], vcc
	v_cndmask_b32_e64 v7, v7, v8, s[4:5]
	v_cndmask_b32_e64 v5, v5, v6, s[4:5]
	v_add_f32_e32 v1, v1, v7
	v_add_f32_e32 v4, v4, v5
	ds_write2_b32 v2, v4, v1 offset0:7 offset1:15
	s_or_b64 exec, exec, s[6:7]
	v_add_f32_dpp v1, v3, v3 quad_perm:[1,0,3,2] row_mask:0xf bank_mask:0xf bound_ctrl:1
	s_nop 1
	v_add_f32_dpp v1, v1, v1 quad_perm:[2,3,0,1] row_mask:0xf bank_mask:0xf bound_ctrl:1
	s_nop 1
	v_add_f32_dpp v1, v1, v1 row_half_mirror row_mask:0xf bank_mask:0xf bound_ctrl:1
	s_nop 1
	v_add_f32_dpp v1, v1, v1 row_mirror row_mask:0xf bank_mask:0xf bound_ctrl:1
	v_mov_b32_e32 v3, v1
	v_mov_b32_e32 v4, v1
	s_nop 1
	v_permlane16_swap_b32_e32 v3, v4
	v_cndmask_b32_e64 v3, v3, v4, s[0:1]
	v_add_f32_e32 v1, v1, v3
	v_mov_b32_e32 v4, v1
	v_mov_b32_e32 v3, v1
	s_nop 1
	v_permlane32_swap_b32_e32 v4, v3
	s_and_saveexec_b64 s[0:1], vcc
	v_add_f32_e32 v1, v1, v3
	ds_write_b32 v2, v1 offset:64
	s_or_b64 exec, exec, s[0:1]
	s_mov_b32 s3, 0
	v_cmp_eq_u32_e32 vcc, 0, v0
	s_waitcnt lgkmcnt(0)
	s_barrier
	s_and_saveexec_b64 s[0:1], vcc
	s_cbranch_execz .LBB6_4
	v_mov_b32_e32 v12, 0
	ds_read2_b32 v[4:5], v12 offset0:16 offset1:80
	ds_read2_b32 v[6:7], v12 offset0:144 offset1:208
	ds_read_b128 v[8:11], v12
	ds_read_b128 v[0:3], v12 offset:16
	ds_read_b128 v[14:17], v12 offset:32
	s_waitcnt lgkmcnt(4)
	v_add_f32_e32 v4, 0, v4
	v_add_f32_e32 v4, v4, v5
	s_waitcnt lgkmcnt(3)
	v_add_f32_e32 v4, v4, v6
	v_add_f32_e32 v13, v4, v7
	ds_read_b128 v[4:7], v12 offset:48
	ds_read_b128 v[18:21], v12 offset:288
	ds_read_b128 v[22:25], v12 offset:256
	ds_read_b128 v[26:29], v12 offset:544
	ds_read_b128 v[30:33], v12 offset:800
	ds_read_b128 v[34:37], v12 offset:304
	s_waitcnt lgkmcnt(6)
	v_pk_add_f32 v[14:15], v[14:15], 0 op_sel_hi:[1,0]
	v_pk_add_f32 v[8:9], v[8:9], 0 op_sel_hi:[1,0]
	s_waitcnt lgkmcnt(4)
	v_pk_add_f32 v[14:15], v[14:15], v[18:19]
	s_waitcnt lgkmcnt(3)
	v_pk_add_f32 v[8:9], v[8:9], v[22:23]
	s_waitcnt lgkmcnt(2)
	v_pk_add_f32 v[14:15], v[14:15], v[26:27]
	ds_read_b128 v[46:49], v12 offset:272
	ds_read_b128 v[50:53], v12 offset:512
	s_waitcnt lgkmcnt(3)
	v_pk_add_f32 v[14:15], v[14:15], v[30:31]
	ds_read_b128 v[38:41], v12 offset:560
	v_div_scale_f32 v18, s[0:1], v13, v13, v15
	v_rcp_f32_e32 v19, v18
	s_waitcnt lgkmcnt(1)
	v_pk_add_f32 v[8:9], v[8:9], v[50:51]
	ds_read_b128 v[42:45], v12 offset:816
	v_pk_add_f32 v[4:5], v[4:5], 0 op_sel_hi:[1,0]
	v_fma_f32 v22, -v18, v19, 1.0
	v_fmac_f32_e32 v19, v22, v19
	v_div_scale_f32 v22, vcc, v15, v13, v15
	v_mul_f32_e32 v23, v22, v19
	v_fma_f32 v26, -v18, v23, v22
	v_fmac_f32_e32 v23, v26, v19
	v_div_scale_f32 v26, s[0:1], v13, v13, v14
	v_rcp_f32_e32 v27, v26
	v_fma_f32 v18, -v18, v23, v22
	v_div_fmas_f32 v18, v18, v19, v23
	ds_read_b128 v[54:57], v12 offset:784
	v_fma_f32 v19, -v26, v27, 1.0
	v_fmac_f32_e32 v27, v19, v27
	v_div_scale_f32 v19, vcc, v14, v13, v14
	v_mul_f32_e32 v22, v19, v27
	v_fma_f32 v23, -v26, v22, v19
	v_fmac_f32_e32 v22, v23, v27
	v_div_fixup_f32 v23, v18, v13, v15
	v_fma_f32 v15, -v26, v22, v19
	v_div_fmas_f32 v15, v15, v27, v22
	v_div_fixup_f32 v22, v15, v13, v14
	v_pk_add_f32 v[18:19], v[16:17], 0 op_sel_hi:[1,0]
	ds_read_b128 v[14:17], v12 offset:768
	v_pk_add_f32 v[26:27], v[18:19], v[20:21]
	v_pk_add_f32 v[4:5], v[4:5], v[34:35]
	ds_read_b128 v[18:21], v12 offset:528
	s_waitcnt lgkmcnt(4)
	v_pk_add_f32 v[4:5], v[4:5], v[38:39]
	s_waitcnt lgkmcnt(1)
	v_pk_add_f32 v[8:9], v[8:9], v[14:15]
	v_pk_add_f32 v[4:5], v[4:5], v[42:43]
	v_div_scale_f32 v14, s[0:1], v13, v13, v9
	v_rcp_f32_e32 v15, v14
	v_pk_add_f32 v[0:1], v[0:1], 0 op_sel_hi:[1,0]
	v_fma_f32 v30, -v14, v15, 1.0
	v_fmac_f32_e32 v15, v30, v15
	v_div_scale_f32 v30, vcc, v9, v13, v9
	v_mul_f32_e32 v31, v30, v15
	v_fma_f32 v50, -v14, v31, v30
	v_fmac_f32_e32 v31, v50, v15
	v_fma_f32 v14, -v14, v31, v30
	v_div_fmas_f32 v14, v14, v15, v31
	v_div_scale_f32 v15, s[0:1], v13, v13, v8
	v_rcp_f32_e32 v30, v15
	v_div_fixup_f32 v9, v14, v13, v9
	v_pk_add_f32 v[0:1], v[0:1], v[46:47]
	v_fma_f32 v31, -v15, v30, 1.0
	v_fmac_f32_e32 v30, v31, v30
	v_div_scale_f32 v31, vcc, v8, v13, v8
	v_mul_f32_e32 v50, v31, v30
	v_fma_f32 v51, -v15, v50, v31
	v_fmac_f32_e32 v50, v51, v30
	v_fma_f32 v15, -v15, v50, v31
	v_div_fmas_f32 v15, v15, v30, v50
	v_div_fixup_f32 v8, v15, v13, v8
	v_pk_mul_f32 v[8:9], v[8:9], v[22:23]
	s_waitcnt lgkmcnt(0)
	v_pk_add_f32 v[0:1], v[0:1], v[18:19]
	v_add_f32_e32 v8, 0, v8
	v_add_f32_e32 v14, v8, v9
	v_pk_add_f32 v[8:9], v[10:11], 0 op_sel_hi:[1,0]
	v_pk_add_f32 v[10:11], v[26:27], v[28:29]
	v_pk_add_f32 v[8:9], v[8:9], v[24:25]
	v_pk_add_f32 v[10:11], v[10:11], v[32:33]
	v_pk_add_f32 v[8:9], v[8:9], v[52:53]
	v_div_scale_f32 v15, s[0:1], v13, v13, v11
	v_rcp_f32_e32 v22, v15
	v_pk_add_f32 v[8:9], v[8:9], v[16:17]
	v_pk_add_f32 v[0:1], v[0:1], v[54:55]
	v_fma_f32 v16, -v15, v22, 1.0
	v_fmac_f32_e32 v22, v16, v22
	v_div_scale_f32 v16, vcc, v11, v13, v11
	v_mul_f32_e32 v17, v16, v22
	v_fma_f32 v23, -v15, v17, v16
	v_fmac_f32_e32 v17, v23, v22
	v_fma_f32 v15, -v15, v17, v16
	v_div_scale_f32 v16, s[0:1], v13, v13, v10
	v_rcp_f32_e32 v23, v16
	v_div_fmas_f32 v15, v15, v22, v17
	v_div_fixup_f32 v11, v15, v13, v11
	v_fma_f32 v15, -v16, v23, 1.0
	v_fmac_f32_e32 v23, v15, v23
	v_div_scale_f32 v15, vcc, v10, v13, v10
	v_mul_f32_e32 v17, v15, v23
	v_fma_f32 v22, -v16, v17, v15
	v_fmac_f32_e32 v17, v22, v23
	v_fma_f32 v15, -v16, v17, v15
	v_div_scale_f32 v16, s[0:1], v13, v13, v9
	v_rcp_f32_e32 v22, v16
	v_div_fmas_f32 v15, v15, v23, v17
	v_div_fixup_f32 v10, v15, v13, v10
	v_fma_f32 v15, -v16, v22, 1.0
	v_fmac_f32_e32 v22, v15, v22
	v_div_scale_f32 v15, vcc, v9, v13, v9
	v_mul_f32_e32 v17, v15, v22
	v_fma_f32 v23, -v16, v17, v15
	v_fmac_f32_e32 v17, v23, v22
	v_fma_f32 v15, -v16, v17, v15
	v_div_scale_f32 v16, s[0:1], v13, v13, v8
	v_rcp_f32_e32 v23, v16
	v_div_fmas_f32 v15, v15, v22, v17
	v_div_fixup_f32 v9, v15, v13, v9
	v_fma_f32 v15, -v16, v23, 1.0
	v_fmac_f32_e32 v23, v15, v23
	v_div_scale_f32 v15, vcc, v8, v13, v8
	v_mul_f32_e32 v17, v15, v23
	v_fma_f32 v22, -v16, v17, v15
	v_fmac_f32_e32 v17, v22, v23
	v_fma_f32 v15, -v16, v17, v15
	v_div_fmas_f32 v15, v15, v23, v17
	v_div_fixup_f32 v8, v15, v13, v8
	v_pk_mul_f32 v[8:9], v[8:9], v[10:11]
	s_nop 0
	v_add_f32_e32 v8, v14, v8
	v_add_f32_e32 v8, v8, v9
	v_div_scale_f32 v9, s[0:1], v13, v13, v5
	v_rcp_f32_e32 v10, v9
	s_nop 0
	v_fma_f32 v11, -v9, v10, 1.0
	v_fmac_f32_e32 v10, v11, v10
	v_div_scale_f32 v11, vcc, v5, v13, v5
	v_mul_f32_e32 v14, v11, v10
	v_fma_f32 v15, -v9, v14, v11
	v_fmac_f32_e32 v14, v15, v10
	v_fma_f32 v9, -v9, v14, v11
	v_div_scale_f32 v11, s[0:1], v13, v13, v4
	v_rcp_f32_e32 v15, v11
	v_div_fmas_f32 v9, v9, v10, v14
	v_div_fixup_f32 v5, v9, v13, v5
	v_fma_f32 v9, -v11, v15, 1.0
	v_fmac_f32_e32 v15, v9, v15
	v_div_scale_f32 v9, vcc, v4, v13, v4
	v_mul_f32_e32 v10, v9, v15
	v_fma_f32 v14, -v11, v10, v9
	v_fmac_f32_e32 v10, v14, v15
	v_fma_f32 v9, -v11, v10, v9
	v_div_scale_f32 v11, s[0:1], v13, v13, v1
	v_rcp_f32_e32 v14, v11
	v_div_fmas_f32 v9, v9, v15, v10
	v_div_fixup_f32 v4, v9, v13, v4
	v_fma_f32 v9, -v11, v14, 1.0
	v_fmac_f32_e32 v14, v9, v14
	v_div_scale_f32 v9, vcc, v1, v13, v1
	v_mul_f32_e32 v10, v9, v14
	v_fma_f32 v15, -v11, v10, v9
	v_fmac_f32_e32 v10, v15, v14
	v_fma_f32 v9, -v11, v10, v9
	v_div_scale_f32 v11, s[0:1], v13, v13, v0
	v_rcp_f32_e32 v15, v11
	v_div_fmas_f32 v9, v9, v14, v10
	v_div_fixup_f32 v1, v9, v13, v1
	v_fma_f32 v9, -v11, v15, 1.0
	v_fmac_f32_e32 v15, v9, v15
	v_div_scale_f32 v9, vcc, v0, v13, v0
	v_mul_f32_e32 v10, v9, v15
	v_fma_f32 v14, -v11, v10, v9
	v_fmac_f32_e32 v10, v14, v15
	v_fma_f32 v9, -v11, v10, v9
	v_div_fmas_f32 v9, v9, v15, v10
	v_div_fixup_f32 v0, v9, v13, v0
	v_pk_mul_f32 v[0:1], v[0:1], v[4:5]
	s_nop 0
	v_add_f32_e32 v0, v8, v0
	v_add_f32_e32 v4, v0, v1
	v_pk_add_f32 v[0:1], v[2:3], 0 op_sel_hi:[1,0]
	v_pk_add_f32 v[2:3], v[6:7], 0 op_sel_hi:[1,0]
	v_pk_add_f32 v[0:1], v[0:1], v[48:49]
	v_pk_add_f32 v[2:3], v[2:3], v[36:37]
	v_pk_add_f32 v[0:1], v[0:1], v[20:21]
	v_pk_add_f32 v[2:3], v[2:3], v[40:41]
	v_pk_add_f32 v[0:1], v[0:1], v[56:57]
	v_pk_add_f32 v[2:3], v[2:3], v[44:45]
	s_nop 0
	v_div_scale_f32 v5, s[0:1], v13, v13, v3
	v_rcp_f32_e32 v6, v5
	s_nop 0
	v_fma_f32 v7, -v5, v6, 1.0
	v_fmac_f32_e32 v6, v7, v6
	v_div_scale_f32 v7, vcc, v3, v13, v3
	v_mul_f32_e32 v8, v7, v6
	v_fma_f32 v9, -v5, v8, v7
	v_fmac_f32_e32 v8, v9, v6
	v_fma_f32 v5, -v5, v8, v7
	v_div_scale_f32 v7, s[0:1], v13, v13, v2
	v_rcp_f32_e32 v9, v7
	v_div_fmas_f32 v5, v5, v6, v8
	v_div_fixup_f32 v3, v5, v13, v3
	v_fma_f32 v5, -v7, v9, 1.0
	v_fmac_f32_e32 v9, v5, v9
	v_div_scale_f32 v5, vcc, v2, v13, v2
	v_mul_f32_e32 v6, v5, v9
	v_fma_f32 v8, -v7, v6, v5
	v_fmac_f32_e32 v6, v8, v9
	v_fma_f32 v5, -v7, v6, v5
	v_div_scale_f32 v7, s[0:1], v13, v13, v1
	v_rcp_f32_e32 v8, v7
	v_div_fmas_f32 v5, v5, v9, v6
	v_div_fixup_f32 v2, v5, v13, v2
	v_fma_f32 v5, -v7, v8, 1.0
	v_fmac_f32_e32 v8, v5, v8
	v_div_scale_f32 v5, vcc, v1, v13, v1
	v_mul_f32_e32 v6, v5, v8
	v_fma_f32 v9, -v7, v6, v5
	v_fmac_f32_e32 v6, v9, v8
	v_fma_f32 v5, -v7, v6, v5
	v_div_scale_f32 v7, s[0:1], v13, v13, v0
	v_rcp_f32_e32 v9, v7
	v_div_fmas_f32 v5, v5, v8, v6
	v_div_fixup_f32 v1, v5, v13, v1
	v_fma_f32 v5, -v7, v9, 1.0
	v_fmac_f32_e32 v9, v5, v9
	v_div_scale_f32 v5, vcc, v0, v13, v0
	v_mul_f32_e32 v6, v5, v9
	v_fma_f32 v8, -v7, v6, v5
	v_fmac_f32_e32 v6, v8, v9
	v_fma_f32 v5, -v7, v6, v5
	v_div_fmas_f32 v5, v5, v9, v6
	v_div_fixup_f32 v0, v5, v13, v0
	v_pk_mul_f32 v[0:1], v[0:1], v[2:3]
	s_nop 0
	v_add_f32_e32 v0, v4, v0
	v_add_f32_e32 v0, v0, v1
	v_mul_f32_e32 v0, 0x41000000, v0
	v_div_scale_f32 v1, s[0:1], v13, v13, v0
	v_rcp_f32_e32 v2, v1
	s_lshl_b64 s[0:1], s[2:3], 2
	s_add_u32 s0, s42, s0
	s_addc_u32 s1, s43, s1
	v_fma_f32 v3, -v1, v2, 1.0
	v_fmac_f32_e32 v2, v3, v2
	v_div_scale_f32 v3, vcc, v0, v13, v0
	v_mul_f32_e32 v4, v3, v2
	v_fma_f32 v5, -v1, v4, v3
	v_fmac_f32_e32 v4, v5, v2
	v_fma_f32 v1, -v1, v4, v3
	v_div_fmas_f32 v1, v1, v2, v4
	v_div_fixup_f32 v0, v1, v13, v0
	global_store_dword v12, v0, s[0:1]
	s_endpgm

	.amdhsa_kernel _Z9tail_up_kPKfPKiS0_S0_PfS0_S2_S3_PK15HIP_vector_typeIfLj4EEiS7_iS3_
		.amdhsa_group_segment_fixed_size 7168
		.amdhsa_private_segment_fixed_size 0
		.amdhsa_kernarg_size 104
		.amdhsa_user_sgpr_count 2
		.amdhsa_user_sgpr_dispatch_ptr 0
		.amdhsa_user_sgpr_queue_ptr 0
		.amdhsa_user_sgpr_kernarg_segment_ptr 1
		.amdhsa_user_sgpr_dispatch_id 0
		.amdhsa_user_sgpr_kernarg_preload_length 0
		.amdhsa_user_sgpr_kernarg_preload_offset 0
		.amdhsa_user_sgpr_private_segment_size 0
		.amdhsa_uses_dynamic_stack 0
		.amdhsa_enable_private_segment 0
		.amdhsa_system_sgpr_workgroup_id_x 1
		.amdhsa_system_sgpr_workgroup_id_y 1
		.amdhsa_system_sgpr_workgroup_id_z 0
		.amdhsa_system_sgpr_workgroup_info 0
		.amdhsa_system_vgpr_workitem_id 0
		.amdhsa_next_free_vgpr 112
		.amdhsa_next_free_sgpr 64
		.amdhsa_accum_offset 112
		.amdhsa_reserve_vcc 1
		.amdhsa_float_round_mode_32 0
		.amdhsa_float_round_mode_16_64 0
		.amdhsa_float_denorm_mode_32 3
		.amdhsa_float_denorm_mode_16_64 3
		.amdhsa_dx10_clamp 1
		.amdhsa_ieee_mode 1
		.amdhsa_fp16_overflow 0
		.amdhsa_tg_split 0
		.amdhsa_exception_fp_ieee_invalid_op 0
		.amdhsa_exception_fp_denorm_src 0
		.amdhsa_exception_fp_ieee_div_zero 0
		.amdhsa_exception_fp_ieee_overflow 0
		.amdhsa_exception_fp_ieee_underflow 0
		.amdhsa_exception_fp_ieee_inexact 0
		.amdhsa_exception_int_div_zero 0
	.end_amdhsa_kernel

.LBB8_2:
	v_add_u32_e32 v65, 0x100, v0
	v_mov_b32_e32 v67, 0
	v_add_u32_e32 v129, 0x200, v0
	v_mov_b32_e32 v131, 0
	v_mul_u32_u24_sdwa v2, v1, s21 dst_sel:DWORD dst_unused:UNUSED_PAD src0_sel:WORD_0 src1_sel:DWORD
	v_lshrrev_b32_e32 v42, 22, v2
	v_mul_lo_u16_e32 v2, 0x60, v42
	v_mul_u32_u24_e32 v4, 0x300, v42
	v_sub_u16_e32 v43, v1, v2
	v_lshlrev_b32_e32 v2, 2, v4
	v_add_u32_e32 v4, s20, v43
	v_ashrrev_i32_e32 v5, 31, v4
	v_lshlrev_b64 v[4:5], 2, v[4:5]
	s_waitcnt lgkmcnt(0)
	v_lshl_add_u64 v[6:7], s[4:5], 0, v[4:5]
	v_lshl_add_u64 v[8:9], s[6:7], 0, v[4:5]
	v_lshl_add_u64 v[6:7], v[6:7], 0, v[2:3]
	global_load_dword v44, v[8:9], off
	v_add_co_u32_e32 v8, vcc, s22, v6
	v_mul_u32_u24_e32 v12, 0x60000, v42
	s_nop 0
	v_addc_co_u32_e32 v9, vcc, 0, v7, vcc
	v_lshlrev_b32_e32 v2, 2, v12
	v_add_co_u32_e32 v12, vcc, s23, v6
	v_lshl_add_u64 v[40:41], s[16:17], 0, v[2:3]
	s_nop 0
	v_addc_co_u32_e32 v13, vcc, 0, v7, vcc
	v_add_co_u32_e32 v14, vcc, s24, v6
	v_lshl_add_u64 v[10:11], s[12:13], 0, v[4:5]
	s_nop 0
	v_addc_co_u32_e32 v15, vcc, 0, v7, vcc
	v_add_co_u32_e32 v16, vcc, s25, v6
	v_lshl_add_u64 v[4:5], v[40:41], 0, v[4:5]
	s_nop 0
	v_addc_co_u32_e32 v17, vcc, 0, v7, vcc
	v_add_co_u32_e32 v18, vcc, s26, v6
	s_nop 1
	v_addc_co_u32_e32 v19, vcc, 0, v7, vcc
	v_add_co_u32_e32 v20, vcc, s27, v6
	s_nop 1
	v_addc_co_u32_e32 v21, vcc, 0, v7, vcc
	v_add_co_u32_e32 v22, vcc, s28, v6
	s_nop 1
	v_addc_co_u32_e32 v23, vcc, 0, v7, vcc
	v_add_co_u32_e32 v24, vcc, s29, v6
	s_nop 1
	v_addc_co_u32_e32 v25, vcc, 0, v7, vcc
	v_add_co_u32_e32 v26, vcc, s30, v6
	s_nop 1
	v_addc_co_u32_e32 v27, vcc, 0, v7, vcc
	v_add_co_u32_e32 v28, vcc, s31, v6
	s_nop 1
	v_addc_co_u32_e32 v29, vcc, 0, v7, vcc
	v_add_co_u32_e32 v30, vcc, s33, v6
	s_nop 1
	v_addc_co_u32_e32 v31, vcc, 0, v7, vcc
	v_add_co_u32_e32 v32, vcc, s34, v6
	s_nop 1
	v_addc_co_u32_e32 v33, vcc, 0, v7, vcc
	v_add_co_u32_e32 v34, vcc, s35, v6
	s_nop 1
	v_addc_co_u32_e32 v35, vcc, 0, v7, vcc
	v_add_co_u32_e32 v36, vcc, s36, v6
	s_nop 1
	v_addc_co_u32_e32 v37, vcc, 0, v7, vcc
	v_add_co_u32_e32 v38, vcc, s37, v6
	s_nop 1
	v_addc_co_u32_e32 v39, vcc, 0, v7, vcc
	global_load_dword v2, v[6:7], off
	global_load_dword v45, v[8:9], off
	global_load_dword v46, v[12:13], off
	global_load_dword v47, v[14:15], off
	global_load_dword v48, v[16:17], off
	global_load_dword v49, v[18:19], off
	global_load_dword v50, v[20:21], off
	global_load_dword v51, v[22:23], off
	global_load_dword v52, v[24:25], off
	global_load_dword v53, v[26:27], off
	global_load_dword v54, v[28:29], off
	global_load_dword v55, v[30:31], off
	global_load_dword v56, v[32:33], off
	global_load_dword v57, v[34:35], off
	global_load_dword v58, v[36:37], off
	global_load_dword v6, v[38:39], off
	global_load_dword v7, v[4:5], off
	global_load_dword v8, v[10:11], off
	v_mul_u32_u24_sdwa v66, v65, s21 dst_sel:DWORD dst_unused:UNUSED_PAD src0_sel:WORD_0 src1_sel:DWORD
	v_lshrrev_b32_e32 v106, 22, v66
	v_mul_lo_u16_e32 v66, 0x60, v106
	v_mul_u32_u24_e32 v68, 0x300, v106
	v_sub_u16_e32 v107, v65, v66
	v_lshlrev_b32_e32 v66, 2, v68
	v_add_u32_e32 v68, s20, v107
	v_ashrrev_i32_e32 v69, 31, v68
	v_lshlrev_b64 v[68:69], 2, v[68:69]
	s_waitcnt lgkmcnt(0)
	v_lshl_add_u64 v[70:71], s[4:5], 0, v[68:69]
	v_lshl_add_u64 v[72:73], s[6:7], 0, v[68:69]
	v_lshl_add_u64 v[70:71], v[70:71], 0, v[66:67]
	global_load_dword v108, v[72:73], off
	v_add_co_u32_e32 v72, vcc, s22, v70
	v_mul_u32_u24_e32 v76, 0x60000, v106
	s_nop 0
	v_addc_co_u32_e32 v73, vcc, 0, v71, vcc
	v_lshlrev_b32_e32 v66, 2, v76
	v_add_co_u32_e32 v76, vcc, s23, v70
	v_lshl_add_u64 v[104:105], s[16:17], 0, v[66:67]
	s_nop 0
	v_addc_co_u32_e32 v77, vcc, 0, v71, vcc
	v_add_co_u32_e32 v78, vcc, s24, v70
	v_lshl_add_u64 v[74:75], s[12:13], 0, v[68:69]
	s_nop 0
	v_addc_co_u32_e32 v79, vcc, 0, v71, vcc
	v_add_co_u32_e32 v80, vcc, s25, v70
	v_lshl_add_u64 v[68:69], v[104:105], 0, v[68:69]
	s_nop 0
	v_addc_co_u32_e32 v81, vcc, 0, v71, vcc
	v_add_co_u32_e32 v82, vcc, s26, v70
	s_nop 1
	v_addc_co_u32_e32 v83, vcc, 0, v71, vcc
	v_add_co_u32_e32 v84, vcc, s27, v70
	s_nop 1
	v_addc_co_u32_e32 v85, vcc, 0, v71, vcc
	v_add_co_u32_e32 v86, vcc, s28, v70
	s_nop 1
	v_addc_co_u32_e32 v87, vcc, 0, v71, vcc
	v_add_co_u32_e32 v88, vcc, s29, v70
	s_nop 1
	v_addc_co_u32_e32 v89, vcc, 0, v71, vcc
	v_add_co_u32_e32 v90, vcc, s30, v70
	s_nop 1
	v_addc_co_u32_e32 v91, vcc, 0, v71, vcc
	v_add_co_u32_e32 v92, vcc, s31, v70
	s_nop 1
	v_addc_co_u32_e32 v93, vcc, 0, v71, vcc
	v_add_co_u32_e32 v94, vcc, s33, v70
	s_nop 1
	v_addc_co_u32_e32 v95, vcc, 0, v71, vcc
	v_add_co_u32_e32 v96, vcc, s34, v70
	s_nop 1
	v_addc_co_u32_e32 v97, vcc, 0, v71, vcc
	v_add_co_u32_e32 v98, vcc, s35, v70
	s_nop 1
	v_addc_co_u32_e32 v99, vcc, 0, v71, vcc
	v_add_co_u32_e32 v100, vcc, s36, v70
	s_nop 1
	v_addc_co_u32_e32 v101, vcc, 0, v71, vcc
	v_add_co_u32_e32 v102, vcc, s37, v70
	s_nop 1
	v_addc_co_u32_e32 v103, vcc, 0, v71, vcc
	global_load_dword v66, v[70:71], off
	global_load_dword v109, v[72:73], off
	global_load_dword v110, v[76:77], off
	global_load_dword v111, v[78:79], off
	global_load_dword v112, v[80:81], off
	global_load_dword v113, v[82:83], off
	global_load_dword v114, v[84:85], off
	global_load_dword v115, v[86:87], off
	global_load_dword v116, v[88:89], off
	global_load_dword v117, v[90:91], off
	global_load_dword v118, v[92:93], off
	global_load_dword v119, v[94:95], off
	global_load_dword v120, v[96:97], off
	global_load_dword v121, v[98:99], off
	global_load_dword v122, v[100:101], off
	global_load_dword v70, v[102:103], off
	global_load_dword v71, v[68:69], off
	global_load_dword v72, v[74:75], off
	v_mul_u32_u24_sdwa v130, v129, s21 dst_sel:DWORD dst_unused:UNUSED_PAD src0_sel:WORD_0 src1_sel:DWORD
	v_lshrrev_b32_e32 v170, 22, v130
	v_mul_lo_u16_e32 v130, 0x60, v170
	v_mul_u32_u24_e32 v132, 0x300, v170
	v_sub_u16_e32 v171, v129, v130
	v_lshlrev_b32_e32 v130, 2, v132
	v_add_u32_e32 v132, s20, v171
	v_ashrrev_i32_e32 v133, 31, v132
	v_lshlrev_b64 v[132:133], 2, v[132:133]
	s_waitcnt lgkmcnt(0)
	v_lshl_add_u64 v[134:135], s[4:5], 0, v[132:133]
	v_lshl_add_u64 v[136:137], s[6:7], 0, v[132:133]
	v_lshl_add_u64 v[134:135], v[134:135], 0, v[130:131]
	global_load_dword v172, v[136:137], off
	v_add_co_u32_e32 v136, vcc, s22, v134
	v_mul_u32_u24_e32 v140, 0x60000, v170
	s_nop 0
	v_addc_co_u32_e32 v137, vcc, 0, v135, vcc
	v_lshlrev_b32_e32 v130, 2, v140
	v_add_co_u32_e32 v140, vcc, s23, v134
	v_lshl_add_u64 v[168:169], s[16:17], 0, v[130:131]
	s_nop 0
	v_addc_co_u32_e32 v141, vcc, 0, v135, vcc
	v_add_co_u32_e32 v142, vcc, s24, v134
	v_lshl_add_u64 v[138:139], s[12:13], 0, v[132:133]
	s_nop 0
	v_addc_co_u32_e32 v143, vcc, 0, v135, vcc
	v_add_co_u32_e32 v144, vcc, s25, v134
	v_lshl_add_u64 v[132:133], v[168:169], 0, v[132:133]
	s_nop 0
	v_addc_co_u32_e32 v145, vcc, 0, v135, vcc
	v_add_co_u32_e32 v146, vcc, s26, v134
	s_nop 1
	v_addc_co_u32_e32 v147, vcc, 0, v135, vcc
	v_add_co_u32_e32 v148, vcc, s27, v134
	s_nop 1
	v_addc_co_u32_e32 v149, vcc, 0, v135, vcc
	v_add_co_u32_e32 v150, vcc, s28, v134
	s_nop 1
	v_addc_co_u32_e32 v151, vcc, 0, v135, vcc
	v_add_co_u32_e32 v152, vcc, s29, v134
	s_nop 1
	v_addc_co_u32_e32 v153, vcc, 0, v135, vcc
	v_add_co_u32_e32 v154, vcc, s30, v134
	s_nop 1
	v_addc_co_u32_e32 v155, vcc, 0, v135, vcc
	v_add_co_u32_e32 v156, vcc, s31, v134
	s_nop 1
	v_addc_co_u32_e32 v157, vcc, 0, v135, vcc
	v_add_co_u32_e32 v158, vcc, s33, v134
	s_nop 1
	v_addc_co_u32_e32 v159, vcc, 0, v135, vcc
	v_add_co_u32_e32 v160, vcc, s34, v134
	s_nop 1
	v_addc_co_u32_e32 v161, vcc, 0, v135, vcc
	v_add_co_u32_e32 v162, vcc, s35, v134
	s_nop 1
	v_addc_co_u32_e32 v163, vcc, 0, v135, vcc
	v_add_co_u32_e32 v164, vcc, s36, v134
	s_nop 1
	v_addc_co_u32_e32 v165, vcc, 0, v135, vcc
	v_add_co_u32_e32 v166, vcc, s37, v134
	s_nop 1
	v_addc_co_u32_e32 v167, vcc, 0, v135, vcc
	global_load_dword v130, v[134:135], off
	global_load_dword v173, v[136:137], off
	global_load_dword v174, v[140:141], off
	global_load_dword v175, v[142:143], off
	global_load_dword v176, v[144:145], off
	global_load_dword v177, v[146:147], off
	global_load_dword v178, v[148:149], off
	global_load_dword v179, v[150:151], off
	global_load_dword v180, v[152:153], off
	global_load_dword v181, v[154:155], off
	global_load_dword v182, v[156:157], off
	global_load_dword v183, v[158:159], off
	global_load_dword v184, v[160:161], off
	global_load_dword v185, v[162:163], off
	global_load_dword v186, v[164:165], off
	global_load_dword v134, v[166:167], off
	global_load_dword v135, v[132:133], off
	global_load_dword v136, v[138:139], off
	v_lshlrev_b32_e32 v4, 2, v43
	v_mad_u32_u24 v4, v42, s38, v4
	s_waitcnt vmcnt(55)
	v_add_f32_e32 v2, 0, v2
	s_waitcnt vmcnt(54)
	v_add_f32_e32 v2, v2, v45
	s_waitcnt vmcnt(53)
	v_add_f32_e32 v2, v2, v46
	s_waitcnt vmcnt(52)
	v_add_f32_e32 v2, v2, v47
	s_waitcnt vmcnt(51)
	v_add_f32_e32 v2, v2, v48
	s_waitcnt vmcnt(50)
	v_add_f32_e32 v2, v2, v49
	s_waitcnt vmcnt(49)
	v_add_f32_e32 v2, v2, v50
	s_waitcnt vmcnt(48)
	v_add_f32_e32 v2, v2, v51
	s_waitcnt vmcnt(47)
	v_add_f32_e32 v2, v2, v52
	s_waitcnt vmcnt(46)
	v_add_f32_e32 v2, v2, v53
	s_waitcnt vmcnt(45)
	v_add_f32_e32 v2, v2, v54
	s_waitcnt vmcnt(44)
	v_add_f32_e32 v2, v2, v55
	s_waitcnt vmcnt(43)
	v_add_f32_e32 v2, v2, v56
	s_waitcnt vmcnt(42)
	v_add_f32_e32 v2, v2, v57
	s_waitcnt vmcnt(41)
	v_add_f32_e32 v2, v2, v58
	s_waitcnt vmcnt(40)
	v_add_f32_e32 v2, v2, v6
	v_add_f32_e32 v2, v2, v44
	s_waitcnt vmcnt(39)
	v_add_f32_e32 v2, v2, v7
	s_waitcnt vmcnt(38)
	v_mul_f32_e32 v5, v2, v8
	ds_write2st64_b32 v4, v5, v2 offset0:160 offset1:175
	v_lshlrev_b32_e32 v68, 2, v107
	v_mad_u32_u24 v68, v106, s38, v68
	s_waitcnt vmcnt(36)
	v_add_f32_e32 v66, 0, v66
	s_waitcnt vmcnt(35)
	v_add_f32_e32 v66, v66, v109
	s_waitcnt vmcnt(34)
	v_add_f32_e32 v66, v66, v110
	s_waitcnt vmcnt(33)
	v_add_f32_e32 v66, v66, v111
	s_waitcnt vmcnt(32)
	v_add_f32_e32 v66, v66, v112
	s_waitcnt vmcnt(31)
	v_add_f32_e32 v66, v66, v113
	s_waitcnt vmcnt(30)
	v_add_f32_e32 v66, v66, v114
	s_waitcnt vmcnt(29)
	v_add_f32_e32 v66, v66, v115
	s_waitcnt vmcnt(28)
	v_add_f32_e32 v66, v66, v116
	s_waitcnt vmcnt(27)
	v_add_f32_e32 v66, v66, v117
	s_waitcnt vmcnt(26)
	v_add_f32_e32 v66, v66, v118
	s_waitcnt vmcnt(25)
	v_add_f32_e32 v66, v66, v119
	s_waitcnt vmcnt(24)
	v_add_f32_e32 v66, v66, v120
	s_waitcnt vmcnt(23)
	v_add_f32_e32 v66, v66, v121
	s_waitcnt vmcnt(22)
	v_add_f32_e32 v66, v66, v122
	s_waitcnt vmcnt(21)
	v_add_f32_e32 v66, v66, v70
	v_add_f32_e32 v66, v66, v108
	s_waitcnt vmcnt(20)
	v_add_f32_e32 v66, v66, v71
	s_waitcnt vmcnt(19)
	v_mul_f32_e32 v69, v66, v72
	ds_write2st64_b32 v68, v69, v66 offset0:160 offset1:175
	v_lshlrev_b32_e32 v132, 2, v171
	v_mad_u32_u24 v132, v170, s38, v132
	s_waitcnt vmcnt(17)
	v_add_f32_e32 v130, 0, v130
	s_waitcnt vmcnt(16)
	v_add_f32_e32 v130, v130, v173
	s_waitcnt vmcnt(15)
	v_add_f32_e32 v130, v130, v174
	s_waitcnt vmcnt(14)
	v_add_f32_e32 v130, v130, v175
	s_waitcnt vmcnt(13)
	v_add_f32_e32 v130, v130, v176
	s_waitcnt vmcnt(12)
	v_add_f32_e32 v130, v130, v177
	s_waitcnt vmcnt(11)
	v_add_f32_e32 v130, v130, v178
	s_waitcnt vmcnt(10)
	v_add_f32_e32 v130, v130, v179
	s_waitcnt vmcnt(9)
	v_add_f32_e32 v130, v130, v180
	s_waitcnt vmcnt(8)
	v_add_f32_e32 v130, v130, v181
	s_waitcnt vmcnt(7)
	v_add_f32_e32 v130, v130, v182
	s_waitcnt vmcnt(6)
	v_add_f32_e32 v130, v130, v183
	s_waitcnt vmcnt(5)
	v_add_f32_e32 v130, v130, v184
	s_waitcnt vmcnt(4)
	v_add_f32_e32 v130, v130, v185
	s_waitcnt vmcnt(3)
	v_add_f32_e32 v130, v130, v186
	s_waitcnt vmcnt(2)
	v_add_f32_e32 v130, v130, v134
	v_add_f32_e32 v130, v130, v172
	s_waitcnt vmcnt(1)
	v_add_f32_e32 v130, v130, v135
	s_waitcnt vmcnt(0)
	v_mul_f32_e32 v133, v130, v136
	ds_write2st64_b32 v132, v133, v130 offset0:160 offset1:175

	.amdhsa_kernel _Z6pool_kPKfS0_S0_S0_S0_S0_PfS1_
		.amdhsa_group_segment_fixed_size 47872
		.amdhsa_private_segment_fixed_size 0
		.amdhsa_kernarg_size 64
		.amdhsa_user_sgpr_count 2
		.amdhsa_user_sgpr_dispatch_ptr 0
		.amdhsa_user_sgpr_queue_ptr 0
		.amdhsa_user_sgpr_kernarg_segment_ptr 1
		.amdhsa_user_sgpr_dispatch_id 0
		.amdhsa_user_sgpr_kernarg_preload_length 0
		.amdhsa_user_sgpr_kernarg_preload_offset 0
		.amdhsa_user_sgpr_private_segment_size 0
		.amdhsa_uses_dynamic_stack 0
		.amdhsa_enable_private_segment 0
		.amdhsa_system_sgpr_workgroup_id_x 1
		.amdhsa_system_sgpr_workgroup_id_y 1
		.amdhsa_system_sgpr_workgroup_id_z 0
		.amdhsa_system_sgpr_workgroup_info 0
		.amdhsa_system_vgpr_workitem_id 0
		.amdhsa_next_free_vgpr 188
		.amdhsa_next_free_sgpr 96
		.amdhsa_accum_offset 188
		.amdhsa_reserve_vcc 1
		.amdhsa_float_round_mode_32 0
		.amdhsa_float_round_mode_16_64 0
		.amdhsa_float_denorm_mode_32 3
		.amdhsa_float_denorm_mode_16_64 3
		.amdhsa_dx10_clamp 1
		.amdhsa_ieee_mode 1
		.amdhsa_fp16_overflow 0
		.amdhsa_tg_split 0
		.amdhsa_exception_fp_ieee_invalid_op 0
		.amdhsa_exception_fp_denorm_src 0
		.amdhsa_exception_fp_ieee_div_zero 0
		.amdhsa_exception_fp_ieee_overflow 0
		.amdhsa_exception_fp_ieee_underflow 0
		.amdhsa_exception_fp_ieee_inexact 0
		.amdhsa_exception_int_div_zero 0
	.end_amdhsa_kernel

.LBB15_1:
	v_mov_b32_e32 v1, v0
	v_mul_u32_u24_sdwa v4, v1, s1 dst_sel:DWORD dst_unused:UNUSED_PAD src0_sel:WORD_0 src1_sel:DWORD
	v_lshrrev_b32_e32 v8, 23, v4
	v_mul_lo_u16_e32 v4, 0xc0, v8
	v_sub_u16_e32 v4, v1, v4
	v_mad_u64_u32 v[6:7], s[14:15], v8, s10, v[2:3]
	v_lshlrev_b32_e32 v4, 2, v4
	v_lshl_add_u64 v[6:7], v[6:7], 0, v[4:5]
	global_load_dword v16, v[6:7], off
	v_mad_u32_u24 v10, v8, s11, v4
	v_add_u32_e32 v1, 0x100, v0
	v_mul_u32_u24_sdwa v4, v1, s1 dst_sel:DWORD dst_unused:UNUSED_PAD src0_sel:WORD_0 src1_sel:DWORD
	v_lshrrev_b32_e32 v8, 23, v4
	v_mul_lo_u16_e32 v4, 0xc0, v8
	v_sub_u16_e32 v4, v1, v4
	v_mad_u64_u32 v[6:7], s[14:15], v8, s10, v[2:3]
	v_lshlrev_b32_e32 v4, 2, v4
	v_lshl_add_u64 v[6:7], v[6:7], 0, v[4:5]
	global_load_dword v17, v[6:7], off
	v_mad_u32_u24 v11, v8, s11, v4
	v_add_u32_e32 v1, 0x200, v0
	v_mul_u32_u24_sdwa v4, v1, s1 dst_sel:DWORD dst_unused:UNUSED_PAD src0_sel:WORD_0 src1_sel:DWORD
	v_lshrrev_b32_e32 v8, 23, v4
	v_mul_lo_u16_e32 v4, 0xc0, v8
	v_sub_u16_e32 v4, v1, v4
	v_mad_u64_u32 v[6:7], s[14:15], v8, s10, v[2:3]
	v_lshlrev_b32_e32 v4, 2, v4
	v_lshl_add_u64 v[6:7], v[6:7], 0, v[4:5]
	global_load_dword v18, v[6:7], off
	v_mad_u32_u24 v12, v8, s11, v4
	v_add_u32_e32 v1, 0x300, v0
	v_mul_u32_u24_sdwa v4, v1, s1 dst_sel:DWORD dst_unused:UNUSED_PAD src0_sel:WORD_0 src1_sel:DWORD
	v_lshrrev_b32_e32 v8, 23, v4
	v_mul_lo_u16_e32 v4, 0xc0, v8
	v_sub_u16_e32 v4, v1, v4
	v_mad_u64_u32 v[6:7], s[14:15], v8, s10, v[2:3]
	v_lshlrev_b32_e32 v4, 2, v4
	v_lshl_add_u64 v[6:7], v[6:7], 0, v[4:5]
	global_load_dword v19, v[6:7], off
	v_mad_u32_u24 v13, v8, s11, v4
	v_add_u32_e32 v1, 0x400, v0
	v_mul_u32_u24_sdwa v4, v1, s1 dst_sel:DWORD dst_unused:UNUSED_PAD src0_sel:WORD_0 src1_sel:DWORD
	v_lshrrev_b32_e32 v8, 23, v4
	v_mul_lo_u16_e32 v4, 0xc0, v8
	v_sub_u16_e32 v4, v1, v4
	v_mad_u64_u32 v[6:7], s[14:15], v8, s10, v[2:3]
	v_lshlrev_b32_e32 v4, 2, v4
	v_lshl_add_u64 v[6:7], v[6:7], 0, v[4:5]
	global_load_dword v20, v[6:7], off
	v_mad_u32_u24 v14, v8, s11, v4
	v_add_u32_e32 v1, 0x500, v0
	v_mul_u32_u24_sdwa v4, v1, s1 dst_sel:DWORD dst_unused:UNUSED_PAD src0_sel:WORD_0 src1_sel:DWORD
	v_lshrrev_b32_e32 v8, 23, v4
	v_mul_lo_u16_e32 v4, 0xc0, v8
	v_sub_u16_e32 v4, v1, v4
	v_mad_u64_u32 v[6:7], s[14:15], v8, s10, v[2:3]
	v_lshlrev_b32_e32 v4, 2, v4
	v_lshl_add_u64 v[6:7], v[6:7], 0, v[4:5]
	global_load_dword v21, v[6:7], off
	v_mad_u32_u24 v15, v8, s11, v4
	s_waitcnt vmcnt(0)
	ds_write_b32 v10, v16 offset:32768
	ds_write_b32 v11, v17 offset:32768
	ds_write_b32 v12, v18 offset:32768
	ds_write_b32 v13, v19 offset:32768
	ds_write_b32 v14, v20 offset:32768
	ds_write_b32 v15, v21 offset:32768
	s_or_b64 exec, exec, s[4:5]
	s_lshl_b32 s4, s2, 6
	s_mul_hi_i32 s1, s0, 0xc00
	s_mulk_i32 s0, 0xc00
	s_ashr_i32 s5, s4, 31
	s_add_u32 s2, s6, s0
	s_addc_u32 s6, s7, s1
	s_lshl_b64 s[0:1], s[4:5], 2
	s_add_u32 s4, s2, s0
	v_lshlrev_b32_e32 v2, 4, v0
	v_lshrrev_b32_e32 v1, 4, v0
	s_addc_u32 s5, s6, s1
	v_and_b32_e32 v50, 0xf0, v2
	v_mov_b32_e32 v51, 0
	v_lshl_add_u64 v[42:43], s[4:5], 0, v[50:51]
	v_mul_u32_u24_e32 v30, 0xc00, v1
	v_mov_b32_e32 v31, v51
	v_lshl_add_u64 v[10:11], v[42:43], 0, v[30:31]
	s_mov_b32 s4, 0xc000
	v_add_co_u32_e32 v12, vcc, s4, v10
	s_mov_b32 s5, 0x18000
	s_nop 0
	v_addc_co_u32_e32 v13, vcc, 0, v11, vcc
	v_add_co_u32_e32 v16, vcc, s5, v10
	s_waitcnt lgkmcnt(0)
	s_barrier
	global_load_dwordx4 v[46:49], v[10:11], off
	s_mov_b32 s6, 0x24000
	v_addc_co_u32_e32 v17, vcc, 0, v11, vcc
	s_movk_i32 s2, 0xc00
	v_mov_b32_e32 v2, 0x3c000
	v_mov_b32_e32 v3, 0x48000
	v_mov_b32_e32 v4, 0x54000
	v_mov_b32_e32 v5, 0x6c000
	v_add_co_u32_e32 v10, vcc, s6, v10
	v_mad_u32_u24 v18, v1, s2, v2
	v_mad_u32_u24 v22, v1, s2, v3
	v_mad_u32_u24 v26, v1, s2, v4
	v_mad_u32_u24 v34, v1, s2, v5
	global_load_dwordx4 v[2:5], v[12:13], off
	global_load_dwordx4 v[6:9], v[16:17], off
	v_addc_co_u32_e32 v11, vcc, 0, v11, vcc
	global_load_dwordx4 v[10:13], v[10:11], off
	v_mov_b32_e32 v15, v51
	v_or_b32_e32 v14, 0x30000, v30
	v_mov_b32_e32 v19, v51
	v_lshl_add_u64 v[14:15], v[42:43], 0, v[14:15]
	v_mov_b32_e32 v23, v51
	global_load_dwordx4 v[14:17], v[14:15], off
	v_lshl_add_u64 v[18:19], v[42:43], 0, v[18:19]
	v_mov_b32_e32 v24, 0x78000
	v_mov_b32_e32 v27, v51
	global_load_dwordx4 v[18:21], v[18:19], off
	v_lshl_add_u64 v[22:23], v[42:43], 0, v[22:23]
	v_mad_u32_u24 v36, v1, s2, v24
	global_load_dwordx4 v[22:25], v[22:23], off
	v_lshl_add_u64 v[26:27], v[42:43], 0, v[26:27]
	global_load_dwordx4 v[26:29], v[26:27], off
	v_or_b32_e32 v30, 0x60000, v30
	v_mov_b32_e32 v35, v51
	v_lshl_add_u64 v[30:31], v[42:43], 0, v[30:31]
	v_mov_b32_e32 v54, 0x84000
	v_mov_b32_e32 v37, v51
	global_load_dwordx4 v[30:33], v[30:31], off
	v_lshl_add_u64 v[44:45], v[42:43], 0, v[34:35]
	v_lshl_add_u64 v[52:53], v[42:43], 0, v[36:37]
	global_load_dwordx4 v[34:37], v[44:45], off
	global_load_dwordx4 v[38:41], v[52:53], off
	v_mad_u32_u24 v44, v1, s2, v54
	v_mov_b32_e32 v45, v51
	v_lshl_add_u64 v[42:43], v[42:43], 0, v[44:45]
	global_load_dwordx4 v[42:45], v[42:43], off
	v_lshlrev_b32_e32 v54, 2, v1
	v_add_u32_e32 v99, 0x8000, v54
	v_add_u32_e32 v125, 0x9000, v54
	ds_read2_b32 v[52:53], v99 offset1:16
	ds_read2_b32 v[80:81], v125 offset0:128 offset1:144
	v_add_u32_e32 v101, 0x8400, v54
	v_add_u32_e32 v103, 0x8800, v54
	v_add_u32_e32 v124, 0x8c00, v54
	v_add_u32_e32 v126, 0x9400, v54
	ds_read2_b32 v[58:59], v99 offset0:192 offset1:208
	ds_read2_b32 v[60:61], v101 offset0:128 offset1:144
	ds_read2_b32 v[68:69], v103 offset0:64 offset1:80
	ds_read2_b32 v[70:71], v124 offset1:16
	ds_read2_b32 v[78:79], v124 offset0:192 offset1:208
	ds_read2_b32 v[82:83], v126 offset0:64 offset1:80
	s_waitcnt lgkmcnt(4)
	v_mov_b32_e32 v100, v61
	v_lshl_or_b32 v1, v1, 11, v50
	v_mov_b32_e32 v98, v59
	s_waitcnt lgkmcnt(3)
	v_mov_b32_e32 v102, v69
	s_movk_i32 s4, 0x200
	v_cmp_gt_u32_e32 vcc, s4, v0
	s_waitcnt vmcnt(11)
	v_pk_fma_f32 v[64:65], v[46:47], v[52:53], 0 op_sel_hi:[1,0,0]
	v_pk_fma_f32 v[74:75], v[48:49], v[52:53], 0 op_sel_hi:[1,0,0]
	v_pk_fma_f32 v[62:63], v[46:47], v[80:81], 0 op_sel_hi:[1,0,0]
	v_pk_fma_f32 v[56:57], v[48:49], v[80:81], 0 op_sel_hi:[1,0,0]
	v_mov_b32_e32 v80, v53
	v_pk_fma_f32 v[84:85], v[46:47], v[58:59], 0 op_sel_hi:[1,0,0]
	v_pk_fma_f32 v[86:87], v[48:49], v[58:59], 0 op_sel_hi:[1,0,0]
	v_pk_fma_f32 v[88:89], v[46:47], v[60:61], 0 op_sel_hi:[1,0,0]
	v_pk_fma_f32 v[90:91], v[48:49], v[60:61], 0 op_sel_hi:[1,0,0]
	v_pk_fma_f32 v[92:93], v[46:47], v[68:69], 0 op_sel_hi:[1,0,0]
	v_pk_fma_f32 v[94:95], v[48:49], v[68:69], 0 op_sel_hi:[1,0,0]
	s_waitcnt lgkmcnt(2)
	v_pk_fma_f32 v[96:97], v[46:47], v[70:71], 0 op_sel_hi:[1,0,0]
	v_pk_fma_f32 v[76:77], v[48:49], v[70:71], 0 op_sel_hi:[1,0,0]
	s_waitcnt lgkmcnt(1)
	v_pk_fma_f32 v[72:73], v[46:47], v[78:79], 0 op_sel_hi:[1,0,0]
	s_waitcnt vmcnt(10)
	v_pk_fma_f32 v[64:65], v[2:3], v[80:81], v[64:65] op_sel_hi:[1,0,1]
	v_pk_fma_f32 v[74:75], v[4:5], v[80:81], v[74:75] op_sel_hi:[1,0,1]
	v_pk_fma_f32 v[66:67], v[48:49], v[78:79], 0 op_sel_hi:[1,0,0]
	s_waitcnt lgkmcnt(0)
	v_pk_fma_f32 v[54:55], v[46:47], v[82:83], 0 op_sel_hi:[1,0,0]
	v_pk_fma_f32 v[46:47], v[48:49], v[82:83], 0 op_sel_hi:[1,0,0]
	v_mov_b32_e32 v78, v71
	v_mov_b32_e32 v48, v83
	ds_read2_b32 v[82:83], v99 offset0:32 offset1:48
	ds_read2_b32 v[104:105], v99 offset0:224 offset1:240
	ds_read2_b32 v[106:107], v101 offset0:160 offset1:176
	ds_read2_b32 v[108:109], v103 offset0:96 offset1:112
	ds_read2_b32 v[110:111], v124 offset0:32 offset1:48
	ds_read2_b32 v[70:71], v124 offset0:224 offset1:240
	ds_read2_b32 v[60:61], v125 offset0:160 offset1:176
	ds_read2_b32 v[52:53], v126 offset0:96 offset1:112
	ds_read2_b32 v[112:113], v99 offset0:64 offset1:80
	ds_read2_b32 v[114:115], v101 offset1:16
	ds_read2_b32 v[116:117], v101 offset0:192 offset1:208
	s_waitcnt vmcnt(9) lgkmcnt(10)
	v_pk_fma_f32 v[64:65], v[6:7], v[82:83], v[64:65] op_sel_hi:[1,0,1]
	v_pk_fma_f32 v[74:75], v[8:9], v[82:83], v[74:75] op_sel_hi:[1,0,1]
	v_mov_b32_e32 v80, v83
	v_mov_b32_e32 v58, v81
	s_waitcnt vmcnt(8)
	v_pk_fma_f32 v[64:65], v[10:11], v[80:81], v[64:65] op_sel_hi:[1,0,1]
	v_pk_fma_f32 v[74:75], v[12:13], v[80:81], v[74:75] op_sel_hi:[1,0,1]
	ds_read2_b32 v[80:81], v99 offset0:96 offset1:112
	s_waitcnt vmcnt(7) lgkmcnt(3)
	v_pk_fma_f32 v[64:65], v[14:15], v[112:113], v[64:65] op_sel_hi:[1,0,1]
	v_pk_fma_f32 v[74:75], v[16:17], v[112:113], v[74:75] op_sel_hi:[1,0,1]
	v_mov_b32_e32 v82, v113
	s_waitcnt vmcnt(6)
	v_pk_fma_f32 v[64:65], v[18:19], v[82:83], v[64:65] op_sel_hi:[1,0,1]
	v_pk_fma_f32 v[74:75], v[20:21], v[82:83], v[74:75] op_sel_hi:[1,0,1]
	ds_read2_b32 v[82:83], v99 offset0:128 offset1:144
	s_waitcnt vmcnt(5) lgkmcnt(1)
	v_pk_fma_f32 v[64:65], v[22:23], v[80:81], v[64:65] op_sel_hi:[1,0,1]
	v_pk_fma_f32 v[74:75], v[24:25], v[80:81], v[74:75] op_sel_hi:[1,0,1]
	v_mov_b32_e32 v80, v81
	s_waitcnt vmcnt(4)
	v_pk_fma_f32 v[64:65], v[26:27], v[80:81], v[64:65] op_sel_hi:[1,0,1]
	v_pk_fma_f32 v[74:75], v[28:29], v[80:81], v[74:75] op_sel_hi:[1,0,1]
	ds_read2_b32 v[80:81], v99 offset0:160 offset1:176
	s_waitcnt vmcnt(3) lgkmcnt(1)
	v_pk_fma_f32 v[64:65], v[30:31], v[82:83], v[64:65] op_sel_hi:[1,0,1]
	v_pk_fma_f32 v[74:75], v[32:33], v[82:83], v[74:75] op_sel_hi:[1,0,1]
	v_mov_b32_e32 v82, v83
	s_waitcnt vmcnt(2)
	v_pk_fma_f32 v[64:65], v[34:35], v[82:83], v[64:65] op_sel_hi:[1,0,1]
	v_pk_fma_f32 v[74:75], v[36:37], v[82:83], v[74:75] op_sel_hi:[1,0,1]
	s_waitcnt vmcnt(1) lgkmcnt(0)
	v_pk_fma_f32 v[64:65], v[38:39], v[80:81], v[64:65] op_sel_hi:[1,0,1]
	v_mov_b32_e32 v82, v81
	v_pk_fma_f32 v[74:75], v[40:41], v[80:81], v[74:75] op_sel_hi:[1,0,1]
	s_waitcnt vmcnt(0)
	v_pk_fma_f32 v[80:81], v[42:43], v[82:83], v[64:65] op_sel_hi:[1,0,1]
	v_pk_fma_f32 v[82:83], v[44:45], v[82:83], v[74:75] op_sel_hi:[1,0,1]
	ds_read2_b32 v[118:119], v103 offset0:128 offset1:144
	ds_read2_b32 v[112:113], v124 offset0:64 offset1:80
	ds_read2_b32 v[120:121], v125 offset1:16
	ds_write_b128 v1, v[80:83]
	ds_read2_b32 v[74:75], v125 offset0:192 offset1:208
	ds_read2_b32 v[64:65], v126 offset0:128 offset1:144
	v_pk_fma_f32 v[80:81], v[2:3], v[98:99], v[84:85] op_sel_hi:[1,0,1]
	v_pk_fma_f32 v[82:83], v[4:5], v[98:99], v[86:87] op_sel_hi:[1,0,1]
	ds_read2_b32 v[84:85], v101 offset0:32 offset1:48
	v_pk_fma_f32 v[80:81], v[6:7], v[104:105], v[80:81] op_sel_hi:[1,0,1]
	v_pk_fma_f32 v[82:83], v[8:9], v[104:105], v[82:83] op_sel_hi:[1,0,1]
	v_mov_b32_e32 v50, v105
	v_pk_fma_f32 v[80:81], v[10:11], v[50:51], v[80:81] op_sel_hi:[1,0,1]
	v_pk_fma_f32 v[82:83], v[12:13], v[50:51], v[82:83] op_sel_hi:[1,0,1]
	v_pk_fma_f32 v[80:81], v[14:15], v[114:115], v[80:81] op_sel_hi:[1,0,1]
	v_pk_fma_f32 v[82:83], v[16:17], v[114:115], v[82:83] op_sel_hi:[1,0,1]
	v_mov_b32_e32 v50, v115
	ds_read2_b32 v[98:99], v101 offset0:64 offset1:80
	v_pk_fma_f32 v[80:81], v[18:19], v[50:51], v[80:81] op_sel_hi:[1,0,1]
	v_pk_fma_f32 v[82:83], v[20:21], v[50:51], v[82:83] op_sel_hi:[1,0,1]
	ds_read2_b32 v[86:87], v101 offset0:224 offset1:240
	s_waitcnt lgkmcnt(2)
	v_pk_fma_f32 v[80:81], v[22:23], v[84:85], v[80:81] op_sel_hi:[1,0,1]
	v_pk_fma_f32 v[82:83], v[24:25], v[84:85], v[82:83] op_sel_hi:[1,0,1]
	v_mov_b32_e32 v50, v85
	ds_read2_b32 v[84:85], v103 offset0:160 offset1:176
	ds_read2_b32 v[104:105], v101 offset0:96 offset1:112
	v_pk_fma_f32 v[80:81], v[26:27], v[50:51], v[80:81] op_sel_hi:[1,0,1]
	v_pk_fma_f32 v[82:83], v[28:29], v[50:51], v[82:83] op_sel_hi:[1,0,1]
	s_waitcnt lgkmcnt(3)
	v_pk_fma_f32 v[80:81], v[30:31], v[98:99], v[80:81] op_sel_hi:[1,0,1]
	v_pk_fma_f32 v[82:83], v[32:33], v[98:99], v[82:83] op_sel_hi:[1,0,1]
	v_mov_b32_e32 v50, v99
	v_pk_fma_f32 v[80:81], v[34:35], v[50:51], v[80:81] op_sel_hi:[1,0,1]
	v_pk_fma_f32 v[82:83], v[36:37], v[50:51], v[82:83] op_sel_hi:[1,0,1]
	s_waitcnt lgkmcnt(0)
	v_pk_fma_f32 v[80:81], v[38:39], v[104:105], v[80:81] op_sel_hi:[1,0,1]
	v_mov_b32_e32 v50, v105
	v_pk_fma_f32 v[82:83], v[40:41], v[104:105], v[82:83] op_sel_hi:[1,0,1]
	v_pk_fma_f32 v[80:81], v[42:43], v[50:51], v[80:81] op_sel_hi:[1,0,1]
	v_pk_fma_f32 v[82:83], v[44:45], v[50:51], v[82:83] op_sel_hi:[1,0,1]
	ds_read2_b32 v[98:99], v124 offset0:96 offset1:112
	ds_read2_b32 v[104:105], v125 offset0:32 offset1:48
	ds_write_b128 v1, v[80:83] offset:256
	v_pk_fma_f32 v[80:81], v[2:3], v[100:101], v[88:89] op_sel_hi:[1,0,1]
	v_pk_fma_f32 v[82:83], v[4:5], v[100:101], v[90:91] op_sel_hi:[1,0,1]
	v_pk_fma_f32 v[80:81], v[6:7], v[106:107], v[80:81] op_sel_hi:[1,0,1]
	v_pk_fma_f32 v[82:83], v[8:9], v[106:107], v[82:83] op_sel_hi:[1,0,1]
	v_mov_b32_e32 v50, v107
	v_pk_fma_f32 v[80:81], v[10:11], v[50:51], v[80:81] op_sel_hi:[1,0,1]
	v_pk_fma_f32 v[82:83], v[12:13], v[50:51], v[82:83] op_sel_hi:[1,0,1]
	ds_read2_b32 v[114:115], v125 offset0:224 offset1:240
	ds_read2_b32 v[122:123], v126 offset0:160 offset1:176
	ds_read2_b32 v[88:89], v103 offset1:16
	v_pk_fma_f32 v[80:81], v[14:15], v[116:117], v[80:81] op_sel_hi:[1,0,1]
	v_pk_fma_f32 v[82:83], v[16:17], v[116:117], v[82:83] op_sel_hi:[1,0,1]
	v_mov_b32_e32 v50, v117
	v_pk_fma_f32 v[80:81], v[18:19], v[50:51], v[80:81] op_sel_hi:[1,0,1]
	v_pk_fma_f32 v[82:83], v[20:21], v[50:51], v[82:83] op_sel_hi:[1,0,1]
	v_pk_fma_f32 v[80:81], v[22:23], v[86:87], v[80:81] op_sel_hi:[1,0,1]
	v_pk_fma_f32 v[82:83], v[24:25], v[86:87], v[82:83] op_sel_hi:[1,0,1]
	v_mov_b32_e32 v50, v87
	ds_read2_b32 v[86:87], v103 offset0:32 offset1:48
	v_pk_fma_f32 v[80:81], v[26:27], v[50:51], v[80:81] op_sel_hi:[1,0,1]
	v_pk_fma_f32 v[82:83], v[28:29], v[50:51], v[82:83] op_sel_hi:[1,0,1]
	s_waitcnt lgkmcnt(1)
	v_pk_fma_f32 v[80:81], v[30:31], v[88:89], v[80:81] op_sel_hi:[1,0,1]
	v_pk_fma_f32 v[82:83], v[32:33], v[88:89], v[82:83] op_sel_hi:[1,0,1]
	v_mov_b32_e32 v50, v89
	v_pk_fma_f32 v[80:81], v[34:35], v[50:51], v[80:81] op_sel_hi:[1,0,1]
	v_pk_fma_f32 v[82:83], v[36:37], v[50:51], v[82:83] op_sel_hi:[1,0,1]
	s_waitcnt lgkmcnt(0)
	v_pk_fma_f32 v[80:81], v[38:39], v[86:87], v[80:81] op_sel_hi:[1,0,1]
	v_mov_b32_e32 v50, v87
	v_pk_fma_f32 v[82:83], v[40:41], v[86:87], v[82:83] op_sel_hi:[1,0,1]
	v_pk_fma_f32 v[80:81], v[42:43], v[50:51], v[80:81] op_sel_hi:[1,0,1]
	v_pk_fma_f32 v[82:83], v[44:45], v[50:51], v[82:83] op_sel_hi:[1,0,1]
	ds_read2_b32 v[90:91], v103 offset0:192 offset1:208
	ds_read2_b32 v[100:101], v124 offset0:128 offset1:144
	ds_read2_b32 v[86:87], v125 offset0:64 offset1:80
	ds_read2_b32 v[88:89], v126 offset1:16
	ds_write_b128 v1, v[80:83] offset:512
	v_pk_fma_f32 v[80:81], v[2:3], v[102:103], v[92:93] op_sel_hi:[1,0,1]
	v_pk_fma_f32 v[92:93], v[4:5], v[102:103], v[94:95] op_sel_hi:[1,0,1]
	v_pk_fma_f32 v[80:81], v[6:7], v[108:109], v[80:81] op_sel_hi:[1,0,1]
	v_pk_fma_f32 v[92:93], v[8:9], v[108:109], v[92:93] op_sel_hi:[1,0,1]
	v_mov_b32_e32 v50, v109
	v_pk_fma_f32 v[80:81], v[10:11], v[50:51], v[80:81] op_sel_hi:[1,0,1]
	v_pk_fma_f32 v[92:93], v[12:13], v[50:51], v[92:93] op_sel_hi:[1,0,1]
	v_pk_fma_f32 v[80:81], v[14:15], v[118:119], v[80:81] op_sel_hi:[1,0,1]
	v_pk_fma_f32 v[92:93], v[16:17], v[118:119], v[92:93] op_sel_hi:[1,0,1]
	v_mov_b32_e32 v50, v119
	v_pk_fma_f32 v[80:81], v[18:19], v[50:51], v[80:81] op_sel_hi:[1,0,1]
	v_pk_fma_f32 v[92:93], v[20:21], v[50:51], v[92:93] op_sel_hi:[1,0,1]
	ds_read2_b32 v[106:107], v126 offset0:192 offset1:208
	ds_read2_b32 v[82:83], v103 offset0:224 offset1:240
	ds_read2_b32 v[116:117], v124 offset0:160 offset1:176
	v_pk_fma_f32 v[80:81], v[22:23], v[84:85], v[80:81] op_sel_hi:[1,0,1]
	v_mov_b32_e32 v50, v85
	v_pk_fma_f32 v[84:85], v[24:25], v[84:85], v[92:93] op_sel_hi:[1,0,1]
	v_pk_fma_f32 v[80:81], v[26:27], v[50:51], v[80:81] op_sel_hi:[1,0,1]
	v_pk_fma_f32 v[84:85], v[28:29], v[50:51], v[84:85] op_sel_hi:[1,0,1]
	s_waitcnt lgkmcnt(7)
	v_pk_fma_f32 v[80:81], v[30:31], v[90:91], v[80:81] op_sel_hi:[1,0,1]
	v_mov_b32_e32 v92, v91
	v_pk_fma_f32 v[84:85], v[32:33], v[90:91], v[84:85] op_sel_hi:[1,0,1]
	v_pk_fma_f32 v[80:81], v[34:35], v[92:93], v[80:81] op_sel_hi:[1,0,1]
	v_pk_fma_f32 v[84:85], v[36:37], v[92:93], v[84:85] op_sel_hi:[1,0,1]
	s_waitcnt lgkmcnt(1)
	v_pk_fma_f32 v[80:81], v[38:39], v[82:83], v[80:81] op_sel_hi:[1,0,1]
	v_mov_b32_e32 v50, v83
	v_pk_fma_f32 v[82:83], v[40:41], v[82:83], v[84:85] op_sel_hi:[1,0,1]
	v_pk_fma_f32 v[80:81], v[42:43], v[50:51], v[80:81] op_sel_hi:[1,0,1]
	v_pk_fma_f32 v[82:83], v[44:45], v[50:51], v[82:83] op_sel_hi:[1,0,1]
	ds_read2_b32 v[94:95], v125 offset0:96 offset1:112
	ds_read2_b32 v[102:103], v126 offset0:32 offset1:48
	ds_read2_b32 v[108:109], v126 offset0:224 offset1:240
	ds_write_b128 v1, v[80:83] offset:768
	v_pk_fma_f32 v[80:81], v[2:3], v[78:79], v[96:97] op_sel_hi:[1,0,1]
	v_pk_fma_f32 v[76:77], v[4:5], v[78:79], v[76:77] op_sel_hi:[1,0,1]
	v_pk_fma_f32 v[80:81], v[6:7], v[110:111], v[80:81] op_sel_hi:[1,0,1]
	v_mov_b32_e32 v50, v111
	v_pk_fma_f32 v[76:77], v[8:9], v[110:111], v[76:77] op_sel_hi:[1,0,1]
	v_pk_fma_f32 v[80:81], v[10:11], v[50:51], v[80:81] op_sel_hi:[1,0,1]
	v_pk_fma_f32 v[76:77], v[12:13], v[50:51], v[76:77] op_sel_hi:[1,0,1]
	v_pk_fma_f32 v[80:81], v[14:15], v[112:113], v[80:81] op_sel_hi:[1,0,1]
	v_mov_b32_e32 v82, v113
	v_pk_fma_f32 v[76:77], v[16:17], v[112:113], v[76:77] op_sel_hi:[1,0,1]
	v_pk_fma_f32 v[80:81], v[18:19], v[82:83], v[80:81] op_sel_hi:[1,0,1]
	v_pk_fma_f32 v[76:77], v[20:21], v[82:83], v[76:77] op_sel_hi:[1,0,1]
	v_mov_b32_e32 v68, v79
	v_pk_fma_f32 v[80:81], v[22:23], v[98:99], v[80:81] op_sel_hi:[1,0,1]
	v_mov_b32_e32 v84, v99
	v_pk_fma_f32 v[76:77], v[24:25], v[98:99], v[76:77] op_sel_hi:[1,0,1]
	v_pk_fma_f32 v[80:81], v[26:27], v[84:85], v[80:81] op_sel_hi:[1,0,1]
	v_pk_fma_f32 v[76:77], v[28:29], v[84:85], v[76:77] op_sel_hi:[1,0,1]
	v_pk_fma_f32 v[72:73], v[2:3], v[68:69], v[72:73] op_sel_hi:[1,0,1]
	v_pk_fma_f32 v[80:81], v[30:31], v[100:101], v[80:81] op_sel_hi:[1,0,1]
	v_mov_b32_e32 v90, v101
	v_pk_fma_f32 v[76:77], v[32:33], v[100:101], v[76:77] op_sel_hi:[1,0,1]
	v_pk_fma_f32 v[72:73], v[6:7], v[70:71], v[72:73] op_sel_hi:[1,0,1]
	v_mov_b32_e32 v50, v71
	v_pk_fma_f32 v[66:67], v[4:5], v[68:69], v[66:67] op_sel_hi:[1,0,1]
	v_pk_fma_f32 v[80:81], v[34:35], v[90:91], v[80:81] op_sel_hi:[1,0,1]
	v_pk_fma_f32 v[76:77], v[36:37], v[90:91], v[76:77] op_sel_hi:[1,0,1]
	v_pk_fma_f32 v[72:73], v[10:11], v[50:51], v[72:73] op_sel_hi:[1,0,1]
	v_pk_fma_f32 v[66:67], v[8:9], v[70:71], v[66:67] op_sel_hi:[1,0,1]
	s_waitcnt lgkmcnt(4)
	v_pk_fma_f32 v[80:81], v[38:39], v[116:117], v[80:81] op_sel_hi:[1,0,1]
	v_mov_b32_e32 v92, v117
	v_pk_fma_f32 v[76:77], v[40:41], v[116:117], v[76:77] op_sel_hi:[1,0,1]
	v_pk_fma_f32 v[72:73], v[14:15], v[120:121], v[72:73] op_sel_hi:[1,0,1]
	v_mov_b32_e32 v78, v121
	v_pk_fma_f32 v[66:67], v[12:13], v[50:51], v[66:67] op_sel_hi:[1,0,1]
	v_pk_fma_f32 v[62:63], v[2:3], v[58:59], v[62:63] op_sel_hi:[1,0,1]
	v_pk_fma_f32 v[56:57], v[4:5], v[58:59], v[56:57] op_sel_hi:[1,0,1]
	v_pk_fma_f32 v[2:3], v[2:3], v[48:49], v[54:55] op_sel_hi:[1,0,1]
	v_pk_fma_f32 v[4:5], v[4:5], v[48:49], v[46:47] op_sel_hi:[1,0,1]
	v_pk_fma_f32 v[80:81], v[42:43], v[92:93], v[80:81] op_sel_hi:[1,0,1]
	v_pk_fma_f32 v[82:83], v[44:45], v[92:93], v[76:77] op_sel_hi:[1,0,1]
	v_pk_fma_f32 v[72:73], v[18:19], v[78:79], v[72:73] op_sel_hi:[1,0,1]
	v_pk_fma_f32 v[66:67], v[16:17], v[120:121], v[66:67] op_sel_hi:[1,0,1]
	v_pk_fma_f32 v[62:63], v[6:7], v[60:61], v[62:63] op_sel_hi:[1,0,1]
	v_mov_b32_e32 v50, v61
	v_pk_fma_f32 v[56:57], v[8:9], v[60:61], v[56:57] op_sel_hi:[1,0,1]
	v_pk_fma_f32 v[2:3], v[6:7], v[52:53], v[2:3] op_sel_hi:[1,0,1]
	v_mov_b32_e32 v6, v53
	v_pk_fma_f32 v[4:5], v[8:9], v[52:53], v[4:5] op_sel_hi:[1,0,1]
	ds_write_b128 v1, v[80:83] offset:1024
	v_pk_fma_f32 v[72:73], v[22:23], v[104:105], v[72:73] op_sel_hi:[1,0,1]
	v_mov_b32_e32 v80, v105
	v_pk_fma_f32 v[66:67], v[20:21], v[78:79], v[66:67] op_sel_hi:[1,0,1]
	v_pk_fma_f32 v[62:63], v[10:11], v[50:51], v[62:63] op_sel_hi:[1,0,1]
	v_pk_fma_f32 v[56:57], v[12:13], v[50:51], v[56:57] op_sel_hi:[1,0,1]
	v_pk_fma_f32 v[2:3], v[10:11], v[6:7], v[2:3] op_sel_hi:[1,0,1]
	v_pk_fma_f32 v[4:5], v[12:13], v[6:7], v[4:5] op_sel_hi:[1,0,1]
	v_pk_fma_f32 v[72:73], v[26:27], v[80:81], v[72:73] op_sel_hi:[1,0,1]
	v_pk_fma_f32 v[66:67], v[24:25], v[104:105], v[66:67] op_sel_hi:[1,0,1]
	v_pk_fma_f32 v[62:63], v[14:15], v[74:75], v[62:63] op_sel_hi:[1,0,1]
	v_mov_b32_e32 v68, v75
	v_pk_fma_f32 v[56:57], v[16:17], v[74:75], v[56:57] op_sel_hi:[1,0,1]
	v_pk_fma_f32 v[2:3], v[14:15], v[64:65], v[2:3] op_sel_hi:[1,0,1]
	v_mov_b32_e32 v10, v65
	v_pk_fma_f32 v[4:5], v[16:17], v[64:65], v[4:5] op_sel_hi:[1,0,1]
	v_pk_fma_f32 v[72:73], v[30:31], v[86:87], v[72:73] op_sel_hi:[1,0,1]
	v_mov_b32_e32 v82, v87
	v_pk_fma_f32 v[66:67], v[28:29], v[80:81], v[66:67] op_sel_hi:[1,0,1]
	v_pk_fma_f32 v[62:63], v[18:19], v[68:69], v[62:63] op_sel_hi:[1,0,1]
	v_pk_fma_f32 v[56:57], v[20:21], v[68:69], v[56:57] op_sel_hi:[1,0,1]
	v_pk_fma_f32 v[2:3], v[18:19], v[10:11], v[2:3] op_sel_hi:[1,0,1]
	v_pk_fma_f32 v[4:5], v[20:21], v[10:11], v[4:5] op_sel_hi:[1,0,1]
	v_pk_fma_f32 v[72:73], v[34:35], v[82:83], v[72:73] op_sel_hi:[1,0,1]
	v_pk_fma_f32 v[66:67], v[32:33], v[86:87], v[66:67] op_sel_hi:[1,0,1]
	v_pk_fma_f32 v[62:63], v[22:23], v[114:115], v[62:63] op_sel_hi:[1,0,1]
	v_mov_b32_e32 v70, v115
	v_pk_fma_f32 v[56:57], v[24:25], v[114:115], v[56:57] op_sel_hi:[1,0,1]
	v_pk_fma_f32 v[2:3], v[22:23], v[122:123], v[2:3] op_sel_hi:[1,0,1]
	v_mov_b32_e32 v14, v123
	v_pk_fma_f32 v[4:5], v[24:25], v[122:123], v[4:5] op_sel_hi:[1,0,1]
	s_waitcnt lgkmcnt(4)
	v_pk_fma_f32 v[72:73], v[38:39], v[94:95], v[72:73] op_sel_hi:[1,0,1]
	v_mov_b32_e32 v84, v95
	v_pk_fma_f32 v[66:67], v[36:37], v[82:83], v[66:67] op_sel_hi:[1,0,1]
	v_pk_fma_f32 v[62:63], v[26:27], v[70:71], v[62:63] op_sel_hi:[1,0,1]
	v_pk_fma_f32 v[56:57], v[28:29], v[70:71], v[56:57] op_sel_hi:[1,0,1]
	v_pk_fma_f32 v[2:3], v[26:27], v[14:15], v[2:3] op_sel_hi:[1,0,1]
	v_pk_fma_f32 v[4:5], v[28:29], v[14:15], v[4:5] op_sel_hi:[1,0,1]
	v_pk_fma_f32 v[76:77], v[42:43], v[84:85], v[72:73] op_sel_hi:[1,0,1]
	v_pk_fma_f32 v[66:67], v[40:41], v[94:95], v[66:67] op_sel_hi:[1,0,1]
	v_pk_fma_f32 v[62:63], v[30:31], v[88:89], v[62:63] op_sel_hi:[1,0,1]
	v_mov_b32_e32 v72, v89
	v_pk_fma_f32 v[56:57], v[32:33], v[88:89], v[56:57] op_sel_hi:[1,0,1]
	v_pk_fma_f32 v[2:3], v[30:31], v[106:107], v[2:3] op_sel_hi:[1,0,1]
	v_mov_b32_e32 v18, v107
	v_pk_fma_f32 v[4:5], v[32:33], v[106:107], v[4:5] op_sel_hi:[1,0,1]
	v_pk_fma_f32 v[78:79], v[44:45], v[84:85], v[66:67] op_sel_hi:[1,0,1]
	v_pk_fma_f32 v[62:63], v[34:35], v[72:73], v[62:63] op_sel_hi:[1,0,1]
	v_pk_fma_f32 v[56:57], v[36:37], v[72:73], v[56:57] op_sel_hi:[1,0,1]
	v_pk_fma_f32 v[2:3], v[34:35], v[18:19], v[2:3] op_sel_hi:[1,0,1]
	v_pk_fma_f32 v[4:5], v[36:37], v[18:19], v[4:5] op_sel_hi:[1,0,1]
	ds_write_b128 v1, v[76:79] offset:1280
	s_waitcnt lgkmcnt(4)
	v_pk_fma_f32 v[62:63], v[38:39], v[102:103], v[62:63] op_sel_hi:[1,0,1]
	v_mov_b32_e32 v76, v103
	v_pk_fma_f32 v[56:57], v[40:41], v[102:103], v[56:57] op_sel_hi:[1,0,1]
	s_waitcnt lgkmcnt(3)
	v_pk_fma_f32 v[2:3], v[38:39], v[108:109], v[2:3] op_sel_hi:[1,0,1]
	v_mov_b32_e32 v22, v109
	v_pk_fma_f32 v[4:5], v[40:41], v[108:109], v[4:5] op_sel_hi:[1,0,1]
	v_pk_fma_f32 v[66:67], v[42:43], v[76:77], v[62:63] op_sel_hi:[1,0,1]
	v_pk_fma_f32 v[68:69], v[44:45], v[76:77], v[56:57] op_sel_hi:[1,0,1]
	v_pk_fma_f32 v[2:3], v[42:43], v[22:23], v[2:3] op_sel_hi:[1,0,1]
	v_pk_fma_f32 v[4:5], v[44:45], v[22:23], v[4:5] op_sel_hi:[1,0,1]
	ds_write_b128 v1, v[66:69] offset:1536
	ds_write_b128 v1, v[2:5] offset:1792
	s_waitcnt lgkmcnt(0)
	s_barrier
	s_and_saveexec_b64 s[4:5], vcc
	s_cbranch_execz .LBB15_5
	s_mul_hi_i32 s4, s3, 0x6000
	s_mulk_i32 s3, 0x6000
	s_add_u32 s0, s0, s3
	v_and_b32_e32 v1, 63, v0
	s_addc_u32 s1, s1, s4
	v_or_b32_e32 v2, 0xffffff00, v0
	v_lshrrev_b32_e32 v4, 6, v0
	v_lshlrev_b32_e32 v50, 2, v1
	v_mov_b64_e32 v[0:1], s[0:1]
	v_mad_u64_u32 v[0:1], s[0:1], v4, s2, v[0:1]
	v_lshl_add_u64 v[0:1], v[0:1], 0, v[50:51]
	v_lshl_or_b32 v3, v4, 8, v50
	v_lshl_add_u64 v[0:1], s[8:9], 0, v[0:1]
	s_mov_b64 s[0:1], 0
	s_mov_b64 s[2:3], 0x3000

amdhsa.kernels:
  - .agpr_count:     0
    .args:
      - .address_space:  global
        .offset:         0
        .size:           8
        .value_kind:     global_buffer
    .group_segment_fixed_size: 0
    .kernarg_segment_align: 8
    .kernarg_segment_size: 8
    .language:       OpenCL C
    .language_version:
      - 2
      - 0
    .max_flat_workgroup_size: 1024
    .name:           _Z7empty_kPi
    .private_segment_fixed_size: 0
    .sgpr_count:     6
    .sgpr_spill_count: 0
    .symbol:         _Z7empty_kPi.kd
    .uniform_work_group_size: 1
    .uses_dynamic_stack: false
    .vgpr_count:     0
    .vgpr_spill_count: 0
    .wavefront_size: 64
  - .agpr_count:     0
    .args:
      - .actual_access:  read_only
        .address_space:  global
        .offset:         0
        .size:           8
        .value_kind:     global_buffer
      - .actual_access:  read_only
        .address_space:  global
        .offset:         8
        .size:           8
        .value_kind:     global_buffer
      - .actual_access:  read_only
        .address_space:  global
        .offset:         16
        .size:           8
        .value_kind:     global_buffer
      - .actual_access:  read_only
        .address_space:  global
        .offset:         24
        .size:           8
        .value_kind:     global_buffer
      - .actual_access:  write_only
        .address_space:  global
        .offset:         32
        .size:           8
        .value_kind:     global_buffer
      - .actual_access:  write_only
        .address_space:  global
        .offset:         40
        .size:           8
        .value_kind:     global_buffer
    .group_segment_fixed_size: 0
    .kernarg_segment_align: 8
    .kernarg_segment_size: 48
    .language:       OpenCL C
    .language_version:
      - 2
      - 0
    .max_flat_workgroup_size: 256
    .name:           _Z4ln_kPKfS0_S0_S0_PfPDF16_
    .private_segment_fixed_size: 0
    .sgpr_count:     19
    .sgpr_spill_count: 0
    .symbol:         _Z4ln_kPKfS0_S0_S0_PfPDF16_.kd
    .uniform_work_group_size: 1
    .uses_dynamic_stack: false
    .vgpr_count:     59
    .vgpr_spill_count: 0
    .wavefront_size: 64
  - .agpr_count:     0
    .args:
      - .actual_access:  read_only
        .address_space:  global
        .offset:         0
        .size:           8
        .value_kind:     global_buffer
      - .actual_access:  read_only
        .address_space:  global
        .offset:         8
        .size:           8
        .value_kind:     global_buffer
      - .actual_access:  read_only
        .address_space:  global
        .offset:         16
        .size:           8
        .value_kind:     global_buffer
      - .actual_access:  read_only
        .address_space:  global
        .offset:         24
        .size:           8
        .value_kind:     global_buffer
      - .actual_access:  read_only
        .address_space:  global
        .offset:         32
        .size:           8
        .value_kind:     global_buffer
      - .actual_access:  write_only
        .address_space:  global
        .offset:         40
        .size:           8
        .value_kind:     global_buffer
      - .actual_access:  write_only
        .address_space:  global
        .offset:         48
        .size:           8
        .value_kind:     global_buffer
      - .actual_access:  write_only
        .address_space:  global
        .offset:         56
        .size:           8
        .value_kind:     global_buffer
      - .actual_access:  write_only
        .address_space:  global
        .offset:         64
        .size:           8
        .value_kind:     global_buffer
      - .offset:         72
        .size:           4
        .value_kind:     by_value
    .group_segment_fixed_size: 24704
    .kernarg_segment_align: 8
    .kernarg_segment_size: 76
    .language:       OpenCL C
    .language_version:
      - 2
      - 0
    .max_flat_workgroup_size: 1024
    .name:           _Z11ln_router_kPKfS0_S0_S0_S0_PfPDF16_PiS1_i
    .private_segment_fixed_size: 0
    .sgpr_count:     34
    .sgpr_spill_count: 0
    .symbol:         _Z11ln_router_kPKfS0_S0_S0_S0_PfPDF16_PiS1_i.kd
    .uniform_work_group_size: 1
    .uses_dynamic_stack: false
    .vgpr_count:     56
    .vgpr_spill_count: 0
    .wavefront_size: 64
  - .agpr_count:     0
    .args:
      - .actual_access:  read_only
        .address_space:  global
        .offset:         0
        .size:           8
        .value_kind:     global_buffer
      - .actual_access:  write_only
        .address_space:  global
        .offset:         8
        .size:           8
        .value_kind:     global_buffer
      - .actual_access:  write_only
        .address_space:  global
        .offset:         16
        .size:           8
        .value_kind:     global_buffer
    .group_segment_fixed_size: 4176
    .kernarg_segment_align: 8
    .kernarg_segment_size: 24
    .language:       OpenCL C
    .language_version:
      - 2
      - 0
    .max_flat_workgroup_size: 1024
    .name:           _Z6sort_kPKiPiS1_
    .private_segment_fixed_size: 0
    .sgpr_count:     102
    .sgpr_spill_count: 0
    .symbol:         _Z6sort_kPKiPiS1_.kd
    .uniform_work_group_size: 1
    .uses_dynamic_stack: false
    .vgpr_count:     48
    .vgpr_spill_count: 0
    .wavefront_size: 64
  - .agpr_count:     0
    .args:
      - .offset:         0
        .size:           272
        .value_kind:     by_value
      - .actual_access:  read_only
        .address_space:  global
        .offset:         272
        .size:           8
        .value_kind:     global_buffer
      - .actual_access:  read_only
        .address_space:  global
        .offset:         280
        .size:           8
        .value_kind:     global_buffer
      - .actual_access:  read_only
        .address_space:  global
        .offset:         288
        .size:           8
        .value_kind:     global_buffer
      - .actual_access:  read_only
        .address_space:  global
        .offset:         296
        .size:           8
        .value_kind:     global_buffer
      - .actual_access:  read_only
        .address_space:  global
        .offset:         304
        .size:           8
        .value_kind:     global_buffer
      - .actual_access:  read_only
        .address_space:  global
        .offset:         312
        .size:           8
        .value_kind:     global_buffer
      - .actual_access:  read_only
        .address_space:  global
        .offset:         320
        .size:           8
        .value_kind:     global_buffer
      - .actual_access:  write_only
        .address_space:  global
        .offset:         328
        .size:           8
        .value_kind:     global_buffer
      - .actual_access:  write_only
        .address_space:  global
        .offset:         336
        .size:           8
        .value_kind:     global_buffer
      - .actual_access:  write_only
        .address_space:  global
        .offset:         344
        .size:           8
        .value_kind:     global_buffer
    .group_segment_fixed_size: 16640
    .kernarg_segment_align: 8
    .kernarg_segment_size: 352
    .language:       OpenCL C
    .language_version:
      - 2
      - 0
    .max_flat_workgroup_size: 256
    .name:           _Z5pre_k7CvtArgsPKiS1_PKfS3_S3_S3_S3_PfPDF16_S4_
    .private_segment_fixed_size: 0
    .sgpr_count:     22
    .sgpr_spill_count: 0
    .symbol:         _Z5pre_k7CvtArgsPKiS1_PKfS3_S3_S3_S3_PfPDF16_S4_.kd
    .uniform_work_group_size: 1
    .uses_dynamic_stack: false
    .vgpr_count:     67
    .vgpr_spill_count: 0
    .wavefront_size: 64
  - .agpr_count:     0
    .args:
      - .actual_access:  read_only
        .address_space:  global
        .offset:         0
        .size:           8
        .value_kind:     global_buffer
      - .actual_access:  read_only
        .address_space:  global
        .offset:         8
        .size:           8
        .value_kind:     global_buffer
      - .actual_access:  read_only
        .address_space:  global
        .offset:         16
        .size:           8
        .value_kind:     global_buffer
      - .actual_access:  read_only
        .address_space:  global
        .offset:         24
        .size:           8
        .value_kind:     global_buffer
      - .actual_access:  write_only
        .address_space:  global
        .offset:         32
        .size:           8
        .value_kind:     global_buffer
      - .actual_access:  read_only
        .address_space:  global
        .offset:         40
        .size:           8
        .value_kind:     global_buffer
      - .offset:         48
        .size:           4
        .value_kind:     by_value
      - .actual_access:  write_only
        .address_space:  global
        .offset:         56
        .size:           8
        .value_kind:     global_buffer
    .group_segment_fixed_size: 133120
    .kernarg_segment_align: 8
    .kernarg_segment_size: 64
    .language:       OpenCL C
    .language_version:
      - 2
      - 0
    .max_flat_workgroup_size: 512
    .name:           _Z6attn_kPKDF16_S0_S0_PKfPDF16_PK15HIP_vector_typeIfLj4EEiPf
    .private_segment_fixed_size: 0
    .sgpr_count:     24
    .sgpr_spill_count: 0
    .symbol:         _Z6attn_kPKDF16_S0_S0_PKfPDF16_PK15HIP_vector_typeIfLj4EEiPf.kd
    .uniform_work_group_size: 1
    .uses_dynamic_stack: false
    .vgpr_count:     110
    .vgpr_spill_count: 0
    .wavefront_size: 64
  - .agpr_count:     0
    .args:
      - .actual_access:  read_only
        .address_space:  global
        .offset:         0
        .size:           8
        .value_kind:     global_buffer
      - .actual_access:  read_only
        .address_space:  global
        .offset:         8
        .size:           8
        .value_kind:     global_buffer
      - .actual_access:  read_only
        .address_space:  global
        .offset:         16
        .size:           8
        .value_kind:     global_buffer
      - .actual_access:  read_only
        .address_space:  global
        .offset:         24
        .size:           8
        .value_kind:     global_buffer
      - .actual_access:  write_only
        .address_space:  global
        .offset:         32
        .size:           8
        .value_kind:     global_buffer
      - .actual_access:  read_only
        .address_space:  global
        .offset:         40
        .size:           8
        .value_kind:     global_buffer
      - .actual_access:  read_only
        .address_space:  global
        .offset:         48
        .size:           8
        .value_kind:     global_buffer
      - .actual_access:  write_only
        .address_space:  global
        .offset:         56
        .size:           8
        .value_kind:     global_buffer
      - .actual_access:  read_only
        .address_space:  global
        .offset:         64
        .size:           8
        .value_kind:     global_buffer
      - .offset:         72
        .size:           4
        .value_kind:     by_value
      - .actual_access:  read_only
        .address_space:  global
        .offset:         80
        .size:           8
        .value_kind:     global_buffer
      - .offset:         88
        .size:           4
        .value_kind:     by_value
      - .actual_access:  write_only
        .address_space:  global
        .offset:         96
        .size:           8
        .value_kind:     global_buffer
    .group_segment_fixed_size: 7168
    .kernarg_segment_align: 8
    .kernarg_segment_size: 104
    .language:       OpenCL C
    .language_version:
      - 2
      - 0
    .max_flat_workgroup_size: 256
    .name:           _Z9tail_up_kPKfPKiS0_S0_PfS0_S2_S3_PK15HIP_vector_typeIfLj4EEiS7_iS3_
    .private_segment_fixed_size: 0
    .sgpr_count:     70
    .sgpr_spill_count: 0
    .symbol:         _Z9tail_up_kPKfPKiS0_S0_PfS0_S2_S3_PK15HIP_vector_typeIfLj4EEiS7_iS3_.kd
    .uniform_work_group_size: 1
    .uses_dynamic_stack: false
    .vgpr_count:     112
    .vgpr_spill_count: 0
    .wavefront_size: 64
  - .agpr_count:     0
    .args:
      - .actual_access:  read_only
        .address_space:  global
        .offset:         0
        .size:           8
        .value_kind:     global_buffer
      - .offset:         8
        .size:           4
        .value_kind:     by_value
      - .actual_access:  read_only
        .address_space:  global
        .offset:         16
        .size:           8
        .value_kind:     global_buffer
      - .actual_access:  read_only
        .address_space:  global
        .offset:         24
        .size:           8
        .value_kind:     global_buffer
      - .actual_access:  read_only
        .address_space:  global
        .offset:         32
        .size:           8
        .value_kind:     global_buffer
      - .actual_access:  read_only
        .address_space:  global
        .offset:         40
        .size:           8
        .value_kind:     global_buffer
      - .actual_access:  write_only
        .address_space:  global
        .offset:         48
        .size:           8
        .value_kind:     global_buffer
    .group_segment_fixed_size: 0
    .kernarg_segment_align: 8
    .kernarg_segment_size: 56
    .language:       OpenCL C
    .language_version:
      - 2
      - 0
    .max_flat_workgroup_size: 512
    .name:           _Z9tail_ln_kPKfiS0_S0_S0_S0_Pf
    .private_segment_fixed_size: 0
    .sgpr_count:     22
    .sgpr_spill_count: 0
    .symbol:         _Z9tail_ln_kPKfiS0_S0_S0_S0_Pf.kd
    .uniform_work_group_size: 1
    .uses_dynamic_stack: false
    .vgpr_count:     48
    .vgpr_spill_count: 0
    .wavefront_size: 64
  - .agpr_count:     0
    .args:
      - .actual_access:  read_only
        .address_space:  global
        .offset:         0
        .size:           8
        .value_kind:     global_buffer
      - .actual_access:  read_only
        .address_space:  global
        .offset:         8
        .size:           8
        .value_kind:     global_buffer
      - .actual_access:  read_only
        .address_space:  global
        .offset:         16
        .size:           8
        .value_kind:     global_buffer
      - .actual_access:  read_only
        .address_space:  global
        .offset:         24
        .size:           8
        .value_kind:     global_buffer
      - .actual_access:  read_only
        .address_space:  global
        .offset:         32
        .size:           8
        .value_kind:     global_buffer
      - .actual_access:  read_only
        .address_space:  global
        .offset:         40
        .size:           8
        .value_kind:     global_buffer
      - .actual_access:  write_only
        .address_space:  global
        .offset:         48
        .size:           8
        .value_kind:     global_buffer
      - .actual_access:  write_only
        .address_space:  global
        .offset:         56
        .size:           8
        .value_kind:     global_buffer
    .group_segment_fixed_size: 47872
    .kernarg_segment_align: 8
    .kernarg_segment_size: 64
    .language:       OpenCL C
    .language_version:
      - 2
      - 0
    .max_flat_workgroup_size: 256
    .name:           _Z6pool_kPKfS0_S0_S0_S0_S0_PfS1_
    .private_segment_fixed_size: 0
    .sgpr_count:     46
    .sgpr_spill_count: 0
    .symbol:         _Z6pool_kPKfS0_S0_S0_S0_S0_PfS1_.kd
    .uniform_work_group_size: 1
    .uses_dynamic_stack: false
    .vgpr_count:     188
    .vgpr_spill_count: 0
    .wavefront_size: 64
  - .agpr_count:     0
    .args:
      - .actual_access:  read_only
        .address_space:  global
        .offset:         0
        .size:           8
        .value_kind:     global_buffer
      - .actual_access:  read_only
        .address_space:  global
        .offset:         8
        .size:           8
        .value_kind:     global_buffer
      - .actual_access:  read_only
        .address_space:  global
        .offset:         16
        .size:           8
        .value_kind:     global_buffer
      - .actual_access:  read_only
        .address_space:  global
        .offset:         24
        .size:           8
        .value_kind:     global_buffer
      - .actual_access:  read_only
        .address_space:  global
        .offset:         32
        .size:           8
        .value_kind:     global_buffer
      - .actual_access:  read_only
        .address_space:  global
        .offset:         40
        .size:           8
        .value_kind:     global_buffer
      - .actual_access:  write_only
        .address_space:  global
        .offset:         48
        .size:           8
        .value_kind:     global_buffer
    .group_segment_fixed_size: 16
    .kernarg_segment_align: 8
    .kernarg_segment_size: 56
    .language:       OpenCL C
    .language_version:
      - 2
      - 0
    .max_flat_workgroup_size: 256
    .name:           _Z8final2_kPKfS0_S0_S0_S0_S0_Pf
    .private_segment_fixed_size: 0
    .sgpr_count:     52
    .sgpr_spill_count: 0
    .symbol:         _Z8final2_kPKfS0_S0_S0_S0_S0_Pf.kd
    .uniform_work_group_size: 1
    .uses_dynamic_stack: false
    .vgpr_count:     67
    .vgpr_spill_count: 0
    .wavefront_size: 64
  - .agpr_count:     0
    .args:
      - .actual_access:  read_only
        .address_space:  global
        .offset:         0
        .size:           8
        .value_kind:     global_buffer
      - .offset:         8
        .size:           4
        .value_kind:     by_value
      - .actual_access:  read_only
        .address_space:  global
        .offset:         16
        .size:           8
        .value_kind:     global_buffer
      - .actual_access:  read_only
        .address_space:  global
        .offset:         24
        .size:           8
        .value_kind:     global_buffer
      - .actual_access:  read_only
        .address_space:  global
        .offset:         32
        .size:           8
        .value_kind:     global_buffer
      - .actual_access:  read_only
        .address_space:  global
        .offset:         40
        .size:           8
        .value_kind:     global_buffer
      - .actual_access:  write_only
        .address_space:  global
        .offset:         48
        .size:           8
        .value_kind:     global_buffer
    .group_segment_fixed_size: 0
    .kernarg_segment_align: 8
    .kernarg_segment_size: 56
    .language:       OpenCL C
    .language_version:
      - 2
      - 0
    .max_flat_workgroup_size: 512
    .name:           _Z7final_kPKfiS0_S0_S0_S0_Pf
    .private_segment_fixed_size: 0
    .sgpr_count:     36
    .sgpr_spill_count: 0
    .symbol:         _Z7final_kPKfiS0_S0_S0_S0_Pf.kd
    .uniform_work_group_size: 1
    .uses_dynamic_stack: false
    .vgpr_count:     20
    .vgpr_spill_count: 0
    .wavefront_size: 64
  - .agpr_count:     0
    .args:
      - .offset:         0
        .size:           136
        .value_kind:     by_value
    .group_segment_fixed_size: 114688
    .kernarg_segment_align: 8
    .kernarg_segment_size: 136
    .language:       OpenCL C
    .language_version:
      - 2
      - 0
    .max_flat_workgroup_size: 512
    .name:           _Z7gemm2_kILi0ELi3ELi1EEv5GArgs
    .private_segment_fixed_size: 0
    .sgpr_count:     43
    .sgpr_spill_count: 0
    .symbol:         _Z7gemm2_kILi0ELi3ELi1EEv5GArgs.kd
    .uniform_work_group_size: 1
    .uses_dynamic_stack: false
    .vgpr_count:     186
    .vgpr_spill_count: 0
    .wavefront_size: 64
  - .agpr_count:     0
    .args:
      - .offset:         0
        .size:           136
        .value_kind:     by_value
    .group_segment_fixed_size: 131072
    .kernarg_segment_align: 8
    .kernarg_segment_size: 136
    .language:       OpenCL C
    .language_version:
      - 2
      - 0
    .max_flat_workgroup_size: 512
    .name:           _Z6gemm_kILi1ELi128ELi4ELi8EEv5GArgs
    .private_segment_fixed_size: 0
    .sgpr_count:     36
    .sgpr_spill_count: 0
    .symbol:         _Z6gemm_kILi1ELi128ELi4ELi8EEv5GArgs.kd
    .uniform_work_group_size: 1
    .uses_dynamic_stack: false
    .vgpr_count:     74
    .vgpr_spill_count: 0
    .wavefront_size: 64
  - .agpr_count:     0
    .args:
      - .offset:         0
        .size:           136
        .value_kind:     by_value
    .group_segment_fixed_size: 81920
    .kernarg_segment_align: 8
    .kernarg_segment_size: 136
    .language:       OpenCL C
    .language_version:
      - 2
      - 0
    .max_flat_workgroup_size: 256
    .name:           _Z6gemm_kILi2ELi128ELi2ELi4EEv5GArgs
    .private_segment_fixed_size: 0
    .sgpr_count:     65
    .sgpr_spill_count: 0
    .symbol:         _Z6gemm_kILi2ELi128ELi2ELi4EEv5GArgs.kd
    .uniform_work_group_size: 1
    .uses_dynamic_stack: false
    .vgpr_count:     194
    .vgpr_spill_count: 0
    .wavefront_size: 64
  - .agpr_count:     0
    .args:
      - .offset:         0
        .size:           136
        .value_kind:     by_value
    .group_segment_fixed_size: 98304
    .kernarg_segment_align: 8
    .kernarg_segment_size: 136
    .language:       OpenCL C
    .language_version:
      - 2
      - 0
    .max_flat_workgroup_size: 512
    .name:           _Z7gemm2_kILi3ELi2ELi2EEv5GArgs
    .private_segment_fixed_size: 0
    .sgpr_count:     36
    .sgpr_spill_count: 0
    .symbol:         _Z7gemm2_kILi3ELi2ELi2EEv5GArgs.kd
    .uniform_work_group_size: 1
    .uses_dynamic_stack: false
    .vgpr_count:     170
    .vgpr_spill_count: 0
    .wavefront_size: 64
  - .agpr_count:     0
    .args:
      - .actual_access:  read_only
        .address_space:  global
        .offset:         0
        .size:           8
        .value_kind:     global_buffer
      - .actual_access:  read_only
        .address_space:  global
        .offset:         8
        .size:           8
        .value_kind:     global_buffer
      - .actual_access:  write_only
        .address_space:  global
        .offset:         16
        .size:           8
        .value_kind:     global_buffer
    .group_segment_fixed_size: 38912
    .kernarg_segment_align: 8
    .kernarg_segment_size: 24
    .language:       OpenCL C
    .language_version:
      - 2
      - 0
    .max_flat_workgroup_size: 256
    .name:           _Z7gemv8_kILi192ELi3072EEvPKfS1_Pf
    .private_segment_fixed_size: 0
    .sgpr_count:     22
    .sgpr_spill_count: 0
    .symbol:         _Z7gemv8_kILi192ELi3072EEvPKfS1_Pf.kd
    .uniform_work_group_size: 1
    .uses_dynamic_stack: false
    .vgpr_count:     127
    .vgpr_spill_count: 0
    .wavefront_size: 64
